# speedup vs baseline: 1.0074x; 1.0074x over previous
_Z6k_mainPKDF16_PKfS2_S2_PKmPjPfS6_:
	s_load_dwordx8 s[52:59], s[0:1], 0x0
	v_and_b32_e32 v5, 63, v0
	v_lshlrev_b32_e32 v1, 4, v5
	s_and_b32 s4, s2, 7
	v_lshlrev_b32_e32 v10, 2, v0
	s_waitcnt lgkmcnt(0)
	global_load_dwordx4 v[6:9], v1, s[58:59]
	v_mbcnt_lo_u32_b32 v1, -1, 0
	v_mbcnt_hi_u32_b32 v132, -1, v1
	v_lshl_or_b32 v1, s4, 12, v10
	global_load_dword v55, v1, s[56:57]
	global_load_dword v56, v1, s[56:57] offset:1024
	global_load_dword v63, v1, s[56:57] offset:2048
	global_load_dword v64, v1, s[56:57] offset:3072
	v_readfirstlane_b32 s28, v0
	s_lshl_b32 s3, s2, 5
	s_load_dwordx8 s[20:27], s[0:1], 0x20
	s_and_b32 s0, s28, 0xffffffc0
	s_and_b32 s1, s3, 0x7fffff00
	s_add_i32 s0, s0, s1
	v_and_b32_e32 v4, 31, v0
	s_lshl_b32 s29, s4, 6
	s_lshl_b32 s1, s0, 4
	v_or_b32_e32 v42, s0, v4
	s_or_b32 s0, s1, s29
	s_ashr_i32 s1, s0, 31
	s_lshl_b64 s[0:1], s[0:1], 6
	s_waitcnt lgkmcnt(0)
	s_add_u32 s0, s20, s0
	s_addc_u32 s1, s21, s1
	s_lshl_b32 s31, s4, 19
	s_add_u32 s4, s52, s31
	v_mov_b32_e32 v3, 0
	v_lshlrev_b32_e32 v2, 4, v0
	s_addc_u32 s5, s53, 0
	s_movk_i32 s8, 0x2000
	v_lshl_add_u64 v[46:47], s[4:5], 0, v[2:3]
	v_add_co_u32_e32 v44, vcc, s8, v46
	s_movk_i32 s9, 0x4000
	s_nop 0
	v_addc_co_u32_e32 v45, vcc, 0, v47, vcc
	v_add_co_u32_e32 v48, vcc, s9, v46
	s_movk_i32 s10, 0x6000
	s_nop 0
	v_addc_co_u32_e32 v49, vcc, 0, v47, vcc
	v_lshlrev_b32_e32 v11, 10, v0
	v_add_co_u32_e32 v50, vcc, s10, v46
	s_mov_b32 s7, 0x8000
	v_and_b32_e32 v10, 0x8000, v11
	v_and_b32_e32 v11, 64, v132
	v_addc_co_u32_e32 v51, vcc, 0, v47, vcc
	v_lshl_or_b32 v61, v4, 7, v10
	v_add_u32_e32 v62, 64, v11
	global_load_dwordx4 v[10:13], v2, s[4:5]
	v_add_co_u32_e32 v52, vcc, s7, v46
	v_xor_b32_e32 v43, 32, v132
	s_nop 0
	v_addc_co_u32_e32 v53, vcc, 0, v47, vcc
	global_load_dwordx4 v[14:17], v[44:45], off offset:-4096
	global_load_dwordx4 v[18:21], v[44:45], off
	global_load_dwordx4 v[22:25], v[48:49], off offset:-4096
	global_load_dwordx4 v[26:29], v[48:49], off
	global_load_dwordx4 v[30:33], v[50:51], off offset:-4096
	global_load_dwordx4 v[34:37], v[50:51], off
	global_load_dwordx4 v[38:41], v[52:53], off offset:-4096
	v_mov_b32_e32 v220, v42
	v_mov_b32_e32 v221, 0
	s_mov_b64 s[94:95], 0x9000
	v_lshl_add_u64 v[222:223], v[220:221], 2, s[54:55]
	v_lshl_add_u64 v[208:209], s[94:95], 0, v[46:47]
	s_mov_b64 s[94:95], 0xb000
	global_load_dword v216, v[222:223], off
	global_load_dword v217, v[222:223], off offset:128
	global_load_dword v218, v61, s[0:1]
	v_lshl_add_u64 v[210:211], s[94:95], 0, v[46:47]
	s_mov_b64 s[94:95], 0xd000
	global_load_dwordx4 v[176:179], v[208:209], off offset:-4096
	global_load_dwordx4 v[180:183], v[208:209], off
	v_lshl_add_u64 v[212:213], s[94:95], 0, v[46:47]
	s_mov_b64 s[94:95], 0xf000
	global_load_dwordx4 v[184:187], v[210:211], off offset:-4096
	global_load_dwordx4 v[188:191], v[210:211], off
	v_lshl_add_u64 v[214:215], s[94:95], 0, v[46:47]
	global_load_dwordx4 v[192:195], v[212:213], off offset:-4096
	global_load_dwordx4 v[196:199], v[212:213], off
	global_load_dwordx4 v[200:203], v[214:215], off offset:-4096
	global_load_dwordx4 v[204:207], v[214:215], off
	v_cmp_lt_i32_e32 vcc, v43, v62
	s_mov_b32 s6, 0x46000000
	v_lshlrev_b32_e32 v54, 1, v0
	v_or_b32_e32 v57, 0x1b000, v54
	v_or_b32_e32 v58, 0x1b800, v54
	v_or_b32_e32 v59, 0x1b200, v54
	v_or_b32_e32 v60, 0x1ba00, v54
	s_movk_i32 s34, 0x90
	s_mov_b32 s4, 0xf000
	s_mov_b32 s30, 0
	s_mov_b32 s7, 0x3e4ccccd
	s_waitcnt vmcnt(23)
	v_max_f32_e32 v1, v9, v9
	v_max_f32_e32 v8, v8, v8
	v_max_f32_e32 v1, v8, v1
	v_max3_f32 v1, v6, v7, v1
	v_cndmask_b32_e32 v7, v132, v43, vcc
	v_lshlrev_b32_e32 v133, 2, v7
	v_mov_b32_dpp v6, v1 quad_perm:[1,0,3,2] row_mask:0xf bank_mask:0xf bound_ctrl:1
	v_max_f32_e32 v6, v6, v6
	v_max_f32_e32 v1, v1, v6
	v_ashrrev_i32_e32 v43, 31, v42
	v_lshl_add_u64 v[8:9], v[42:43], 2, s[54:55]
	v_mov_b32_dpp v6, v1 quad_perm:[2,3,0,1] row_mask:0xf bank_mask:0xf bound_ctrl:1
	v_max_f32_e32 v6, v6, v6
	v_max_f32_e32 v1, v1, v6
	s_nop 1
	v_mov_b32_dpp v6, v1 row_half_mirror row_mask:0xf bank_mask:0xf bound_ctrl:1
	v_max_f32_e32 v6, v6, v6
	v_max_f32_e32 v1, v1, v6
	s_nop 1
	v_mov_b32_dpp v6, v1 row_mirror row_mask:0xf bank_mask:0xf bound_ctrl:1
	v_max_f32_e32 v6, v6, v6
	v_max_f32_e32 v1, v1, v6
	ds_swizzle_b32 v6, v1 offset:swizzle(SWAP,16)
	s_waitcnt lgkmcnt(0)
	v_max_f32_e32 v6, v6, v6
	v_max_f32_e32 v7, v1, v6
	ds_bpermute_b32 v44, v133, v7
	s_waitcnt lgkmcnt(0)
	v_max_f32_e32 v8, v44, v44
	v_max_f32_e32 v7, v7, v8
	s_waitcnt vmcnt(22)
	v_sub_f32_e32 v8, v55, v7
	s_waitcnt vmcnt(21)
	v_sub_f32_e32 v9, v56, v7
	v_mul_f32_e32 v42, 0x3fb8aa3b, v8
	v_mul_f32_e32 v8, 0x3e4ccccd, v8
	v_mul_f32_e32 v43, 0x3fb8aa3b, v9
	v_mul_f32_e32 v9, 0x3e4ccccd, v9
	v_mul_f32_e32 v8, 0x3fb8aa3b, v8
	v_mul_f32_e32 v9, 0x3fb8aa3b, v9
	v_exp_f32_e32 v8, v8
	v_exp_f32_e32 v42, v42
	v_exp_f32_e32 v9, v9
	v_exp_f32_e32 v43, v43
	v_cvt_f16_f32_e32 v8, v8
	v_fma_mixlo_f16 v42, v42, s6, 0
	v_cvt_f16_f32_e32 v9, v9
	v_fma_mixlo_f16 v43, v43, s6, 0
	ds_write_b16 v57, v42
	ds_write_b16 v59, v43
	ds_write_b16 v58, v8
	ds_write_b16 v60, v9
	s_waitcnt vmcnt(20)
	v_sub_f32_e32 v8, v63, v7
	v_mul_f32_e32 v9, 0x3fb8aa3b, v8
	v_exp_f32_e32 v9, v9
	v_mul_f32_e32 v8, 0x3e4ccccd, v8
	v_or_b32_e32 v42, 0x1b400, v54
	v_mul_f32_e32 v8, 0x3fb8aa3b, v8
	v_fma_mixlo_f16 v9, v9, s6, 0
	ds_write_b16 v42, v9
	s_waitcnt vmcnt(19)
	v_sub_f32_e32 v9, v64, v7
	v_exp_f32_e32 v8, v8
	v_mul_f32_e32 v42, 0x3fb8aa3b, v9
	v_mul_f32_e32 v9, 0x3e4ccccd, v9
	v_mul_f32_e32 v9, 0x3fb8aa3b, v9
	v_exp_f32_e32 v9, v9
	v_cvt_f16_f32_e32 v8, v8
	v_exp_f32_e32 v42, v42
	v_or_b32_e32 v43, 0x1bc00, v54
	v_cvt_f16_f32_e32 v9, v9
	ds_write_b16 v43, v8
	v_fma_mixlo_f16 v8, v42, s6, 0
	v_or_b32_e32 v42, 0x1b600, v54
	ds_write_b16 v42, v8
	v_or_b32_e32 v8, 0x1be00, v54
	ds_write_b16 v8, v9
	v_lshrrev_b32_e32 v8, 3, v0
	v_and_b32_e32 v9, 0x70, v2
	v_mad_u32_u24 v144, v8, s34, v9
	v_add_co_u32_e32 v8, vcc, s4, v46
	s_mov_b32 s4, 0xa000
	s_nop 0
	v_addc_co_u32_e32 v9, vcc, 0, v47, vcc
	s_waitcnt vmcnt(18)
	ds_write_b128 v144, v[10:13]
	s_waitcnt vmcnt(17)
	ds_write_b128 v144, v[14:17] offset:4608
	s_waitcnt vmcnt(16)
	ds_write_b128 v144, v[18:21] offset:9216
	s_waitcnt vmcnt(15)
	ds_write_b128 v144, v[22:25] offset:13824
	s_waitcnt vmcnt(14)
	ds_write_b128 v144, v[26:29] offset:18432
	s_waitcnt vmcnt(13)
	ds_write_b128 v144, v[30:33] offset:23040
	s_waitcnt vmcnt(12)
	ds_write_b128 v144, v[34:37] offset:27648
	v_add_co_u32_e32 v20, vcc, s4, v46
	s_mov_b32 s4, 0xc000
	s_nop 0
	v_addc_co_u32_e32 v21, vcc, 0, v47, vcc
	v_add_co_u32_e32 v28, vcc, s4, v46
	s_mov_b32 s4, 0xe000
	s_nop 0
	v_addc_co_u32_e32 v29, vcc, 0, v47, vcc
	v_add_co_u32_e32 v36, vcc, s4, v46
	s_waitcnt vmcnt(11)
	ds_write_b128 v144, v[38:41] offset:32256
	v_addc_co_u32_e32 v37, vcc, 0, v47, vcc
	s_nop 0
	s_nop 0
	v_mov_b32_e32 v36, v3
	v_mov_b32_e32 v37, v3
	v_mov_b32_e32 v38, v3
	v_mov_b32_e32 v39, v3
	s_mov_b32 s4, 0x9e3779b9
	s_waitcnt vmcnt(8)
	v_cmp_eq_u32_e32 vcc, s4, v218
	v_mfma_f32_32x32x16_f16 a[0:15], v[36:39], v[36:39], 0
	v_add_u32_e32 v40, 0x10e00, v144
	v_mfma_f32_32x32x16_f16 a[16:31], v[36:39], v[36:39], 0
	s_nop 0
	v_mfma_f32_32x32x16_f16 a[32:47], v[36:39], v[36:39], 0
	s_nop 0
	v_mfma_f32_32x32x16_f16 a[48:63], v[36:39], v[36:39], 0
	s_nop 0
	v_mfma_f32_32x32x16_f16 a[64:79], v[36:39], v[36:39], 0
	s_nop 0
	v_mfma_f32_32x32x16_f16 a[112:127], v[36:39], v[36:39], 0
	s_nop 0
	v_mfma_f32_32x32x16_f16 a[128:143], v[36:39], v[36:39], 0
	s_nop 0
	v_mfma_f32_32x32x16_f16 a[80:95], v[36:39], v[36:39], 0
	s_nop 0
	v_mfma_f32_32x32x16_f16 a[240:255], v[36:39], v[36:39], 0
	s_nop 0
	v_mfma_f32_32x32x16_f16 a[224:239], v[36:39], v[36:39], 0
	s_nop 0
	v_mfma_f32_32x32x16_f16 a[208:223], v[36:39], v[36:39], 0
	s_nop 0
	v_mfma_f32_32x32x16_f16 a[192:207], v[36:39], v[36:39], 0
	s_nop 0
	v_mfma_f32_32x32x16_f16 a[176:191], v[36:39], v[36:39], 0
	s_nop 0
	v_mfma_f32_32x32x16_f16 a[160:175], v[36:39], v[36:39], 0
	s_nop 0
	v_mfma_f32_32x32x16_f16 a[144:159], v[36:39], v[36:39], 0
	s_waitcnt vmcnt(7)
	ds_write_b128 v144, v[176:179] offset:36864
	s_waitcnt vmcnt(6)
	ds_write_b128 v144, v[180:183] offset:41472
	s_waitcnt vmcnt(5)
	ds_write_b128 v144, v[184:187] offset:46080
	s_waitcnt vmcnt(4)
	ds_write_b128 v144, v[188:191] offset:50688
	s_waitcnt vmcnt(3)
	ds_write_b128 v144, v[192:195] offset:55296
	s_waitcnt vmcnt(2)
	ds_write_b128 v144, v[196:199] offset:59904
	s_waitcnt vmcnt(1)
	ds_write_b128 v144, v[200:203] offset:64512
	s_waitcnt vmcnt(0)
	ds_write_b128 v40, v[204:207]
	v_mfma_f32_32x32x16_f16 a[96:111], v[36:39], v[36:39], 0
	s_and_saveexec_b64 s[4:5], vcc
	s_cbranch_execz .LBB1_2
	s_nop 0
.LBB1_2:
	s_or_b64 exec, exec, s[4:5]
	v_add_f32_e32 v1, v7, v216
	v_max_f32_e32 v8, 0, v1
	v_sub_f32_e32 v9, v1, v8
	v_fma_f32 v1, v1, s7, -v8
	v_mul_f32_e32 v1, 0x3fb8aa3b, v1
	v_mul_f32_e32 v8, 0xbfb8aa3b, v8
	v_exp_f32_e32 v1, v1
	v_exp_f32_e32 v8, v8
	v_add_f32_e32 v6, v7, v217
	v_max_f32_e32 v7, 0, v6
	v_mul_f32_e32 v10, 0x46000000, v1
	v_fma_mixlo_f16 v15, v1, s6, 0
	v_mul_f32_e32 v1, 0x46000000, v8
	v_sub_f32_e32 v8, v6, v7
	v_fma_f32 v6, v6, s7, -v7
	v_mul_f32_e32 v9, 0x3fb8aa3b, v9
	v_mul_f32_e32 v6, 0x3fb8aa3b, v6
	v_mul_f32_e32 v7, 0xbfb8aa3b, v7
	v_exp_f32_e32 v9, v9
	v_exp_f32_e32 v6, v6
	v_exp_f32_e32 v7, v7
	v_mul_f32_e32 v8, 0x3fb8aa3b, v8
	v_lshrrev_b32_e32 v5, 1, v5
	v_exp_f32_e32 v16, v8
	v_and_b32_e32 v5, 16, v5
	v_or_b32_e32 v142, 0x1b000, v5
	v_cvt_f16_f32_e32 v14, v9
	v_cvt_pk_f16_f32 v136, v9, v9
	v_cvt_pk_f16_f32 v137, v10, v10
	v_mul_f32_e32 v18, 0x46000000, v6
	v_fma_mixlo_f16 v22, v6, s6, 0
	v_mul_f32_e32 v19, 0x46000000, v7
	s_waitcnt lgkmcnt(0)
	s_barrier
	v_or_b32_e32 v143, 0x1b800, v5
	ds_read_b128 v[6:9], v142
	ds_read_b128 v[10:13], v143
	v_cvt_f16_f32_e32 v17, v16
	s_load_dwordx16 s[4:19], s[0:1], 0x0
	v_cvt_pk_f16_f32 v140, v16, v16
	v_cvt_pk_f16_f32 v139, v18, v18
	s_waitcnt lgkmcnt(0)
	v_pk_mul_f16 v16, v6, v14 op_sel_hi:[1,0]
	v_pk_mul_f16 v18, v10, v15 op_sel_hi:[1,0]
	v_cvt_pk_f16_f32 v1, v1, v1
	v_pk_max_f16 v16, v16, v18
	v_pk_mul_f16 v6, v6, v17 op_sel_hi:[1,0]
	v_pk_mul_f16 v10, v10, v22 op_sel_hi:[1,0]
	s_mov_b32 s33, 0x7060100
	v_pk_max_f16 v6, v6, v10
	v_cndmask_b32_e64 v10, v1, v16, s[4:5]
	v_cndmask_b32_e64 v16, v1, v16, s[6:7]
	v_perm_b32 v18, v16, v10, s33
	v_pk_mul_f16 v10, v7, v14 op_sel_hi:[1,0]
	v_pk_mul_f16 v16, v11, v15 op_sel_hi:[1,0]
	v_cvt_pk_f16_f32 v138, v19, v19
	v_pk_max_f16 v10, v10, v16
	s_load_dwordx16 s[36:51], s[0:1], 0x8000
	v_cndmask_b32_e64 v16, v1, v10, s[8:9]
	v_cndmask_b32_e64 v10, v1, v10, s[10:11]
	v_perm_b32 v19, v10, v16, s33
	v_pk_mul_f16 v10, v8, v14 op_sel_hi:[1,0]
	v_pk_mul_f16 v16, v12, v15 op_sel_hi:[1,0]
	v_pk_mul_f16 v7, v7, v17 op_sel_hi:[1,0]
	v_pk_max_f16 v10, v10, v16
	v_pk_mul_f16 v11, v11, v22 op_sel_hi:[1,0]
	v_cndmask_b32_e64 v16, v1, v10, s[12:13]
	v_cndmask_b32_e64 v10, v1, v10, s[14:15]
	v_perm_b32 v20, v10, v16, s33
	v_pk_mul_f16 v10, v9, v14 op_sel_hi:[1,0]
	v_pk_mul_f16 v14, v13, v15 op_sel_hi:[1,0]
	v_pk_mul_f16 v8, v8, v17 op_sel_hi:[1,0]
	v_pk_max_f16 v10, v10, v14
	v_pk_mul_f16 v12, v12, v22 op_sel_hi:[1,0]
	v_cndmask_b32_e64 v14, v1, v10, s[16:17]
	v_cndmask_b32_e64 v10, v1, v10, s[18:19]
	v_perm_b32 v21, v10, v14, s33
	v_pk_add_f16 v10, v19, v18
	v_pk_add_f16 v14, v20, v21
	v_pk_mul_f16 v9, v9, v17 op_sel_hi:[1,0]
	v_pk_mul_f16 v13, v13, v22 op_sel_hi:[1,0]
	v_pk_add_f16 v10, v10, v14
	v_mov_b32_e32 v134, v3
	v_pk_max_f16 v7, v7, v11
	v_pk_max_f16 v8, v8, v12
	v_pk_max_f16 v9, v9, v13
	v_dot2c_f32_f16_e32 v134, 0x3c003c00, v10
	s_waitcnt lgkmcnt(0)
	v_cndmask_b32_e64 v10, v138, v6, s[36:37]
	v_cndmask_b32_e64 v6, v138, v6, s[38:39]
	v_cndmask_b32_e64 v11, v138, v7, s[40:41]
	v_cndmask_b32_e64 v7, v138, v7, s[42:43]
	v_cndmask_b32_e64 v12, v138, v8, s[44:45]
	v_cndmask_b32_e64 v8, v138, v8, s[46:47]
	v_cndmask_b32_e64 v13, v138, v9, s[48:49]
	v_cndmask_b32_e64 v9, v138, v9, s[50:51]
	v_perm_b32 v38, v6, v10, s33
	v_perm_b32 v39, v7, v11, s33
	v_perm_b32 v40, v8, v12, s33
	v_perm_b32 v41, v9, v13, s33
	v_pk_add_f16 v6, v39, v38
	v_pk_add_f16 v7, v40, v41
	v_mov_b32_e32 v135, v3
	v_pk_add_f16 v6, v6, v7
	v_mad_u32_u24 v141, v4, s34, v5
	v_dot2c_f32_f16_e32 v135, 0x3c003c00, v6
	v_or_b32_e32 v6, 0x1b020, v5
	s_load_dwordx16 s[36:51], s[0:1], 0x40
	s_load_dwordx16 s[4:19], s[0:1], 0x8040
	v_or_b32_e32 v7, 0x1b820, v5
	ds_read_b128 v[46:49], v6
	ds_read_b128 v[42:45], v7
	ds_read_b128 v[74:77], v141
	ds_read_b128 v[126:129], v141 offset:4608
	ds_read_b128 v[122:125], v141 offset:9216
	ds_read_b128 v[118:121], v141 offset:13824
	ds_read_b128 v[106:109], v141 offset:18432
	ds_read_b128 v[98:101], v141 offset:23040
	ds_read_b128 v[94:97], v141 offset:27648
	ds_read_b128 v[86:89], v141 offset:32256
	s_add_u32 s34, s52, s31
	s_addc_u32 s35, s53, 0
	s_lshl_b32 s31, s2, 9
	s_lshl_b32 s28, s28, 4
	s_and_b32 s31, s31, 0xfffff000
	s_and_b32 s28, s28, 0xfffffc00
	s_add_i32 s31, s31, s28
	s_or_b32 s28, s31, s29
	s_ashr_i32 s29, s28, 31
	v_lshl_add_u64 v[2:3], s[34:35], 0, v[2:3]
	s_mov_b64 s[34:35], 0x1700c
	s_lshl_b64 s[28:29], s[28:29], 6
	v_lshl_add_u64 v[130:131], v[2:3], 0, s[34:35]
	s_add_u32 s35, s20, s28
	v_or_b32_e32 v145, 0x1b040, v5
	s_movk_i32 s34, 0xf000
	s_addc_u32 s84, s21, s29
	s_mov_b64 s[20:21], 0
	s_movk_i32 s85, 0x9000
	s_movk_i32 s86, 0xa000
	s_movk_i32 s87, 0xb000
	s_movk_i32 s88, 0xc000
	s_movk_i32 s89, 0xd000
	s_movk_i32 s90, 0xe000
	s_mov_b64 s[28:29], 0x8000
.LBB1_3:
	v_add_co_u32_e32 v2, vcc, s85, v130
	global_load_dwordx4 v[34:37], v[130:131], off offset:-12
	s_nop 0
	v_addc_co_u32_e32 v3, vcc, -1, v131, vcc
	v_add_co_u32_e32 v4, vcc, s86, v130
	global_load_dwordx4 v[6:9], v[2:3], off offset:-12
	s_nop 0
	v_addc_co_u32_e32 v5, vcc, -1, v131, vcc
	v_add_co_u32_e32 v10, vcc, s87, v130
	global_load_dwordx4 v[2:5], v[4:5], off offset:-12
	s_nop 0
	v_addc_co_u32_e32 v11, vcc, -1, v131, vcc
	v_add_co_u32_e32 v12, vcc, s88, v130
	global_load_dwordx4 v[14:17], v[10:11], off offset:-12
	s_nop 0
	v_addc_co_u32_e32 v13, vcc, -1, v131, vcc
	v_add_co_u32_e32 v22, vcc, s89, v130
	global_load_dwordx4 v[10:13], v[12:13], off offset:-12
	s_nop 0
	v_addc_co_u32_e32 v23, vcc, -1, v131, vcc
	v_add_co_u32_e32 v24, vcc, s90, v130
	global_load_dwordx4 v[26:29], v[22:23], off offset:-12
	s_nop 0
	v_addc_co_u32_e32 v25, vcc, -1, v131, vcc
	v_add_co_u32_e32 v30, vcc, s34, v130
	global_load_dwordx4 v[22:25], v[24:25], off offset:-12
	s_nop 0
	v_addc_co_u32_e32 v31, vcc, -1, v131, vcc
	global_load_dwordx4 v[30:33], v[30:31], off offset:-12
	s_waitcnt lgkmcnt(0)
	v_mfma_f32_32x32x16_f16 a[0:15], v[18:21], v[74:77], a[0:15]
	s_add_i32 s31, s30, 1
	s_cmp_lg_u32 s30, 2
	s_cselect_b32 s91, s31, 0
	s_mul_i32 s30, s30, 0x9000
	s_mul_i32 s92, s91, 0x9000
	v_add_u32_e32 v147, s30, v141
	v_add_u32_e32 v146, s92, v141
	s_add_u32 s30, s35, s20
	s_addc_u32 s31, s84, s21
	s_load_dwordx16 s[68:83], s[30:31], 0x80
	s_load_dwordx16 s[52:67], s[30:31], 0x8080
	ds_read_b128 v[90:93], v145
	ds_read_b128 v[82:85], v145 offset:2048
	v_mfma_f32_32x32x16_f16 a[240:255], v[38:41], v[74:77], a[240:255]
	ds_read_b128 v[50:53], v147 offset:32
	v_pk_mul_f16 v148, v46, v136
	v_pk_mul_f16 v149, v42, v137
	v_pk_mul_f16 v150, v47, v136
	v_pk_mul_f16 v151, v43, v137
	v_mfma_f32_32x32x16_f16 a[16:31], v[18:21], v[126:129], a[16:31]
	ds_read_b128 v[54:57], v147 offset:4640
	v_pk_max_f16 v148, v148, v149
	v_pk_max_f16 v150, v150, v151
	v_cndmask_b32_e64 v149, v1, v148, s[36:37]
	v_cndmask_b32_e64 v148, v1, v148, s[38:39]
	v_mfma_f32_32x32x16_f16 a[224:239], v[38:41], v[126:129], a[224:239]
	ds_read_b128 v[58:61], v147 offset:9248
	v_perm_b32 v114, v148, v149, s33
	v_cndmask_b32_e64 v151, v1, v150, s[40:41]
	v_cndmask_b32_e64 v150, v1, v150, s[42:43]
	v_perm_b32 v115, v150, v151, s33
	v_mfma_f32_32x32x16_f16 a[32:47], v[18:21], v[122:125], a[32:47]
	ds_read_b128 v[62:65], v147 offset:13856
	v_pk_mul_f16 v148, v48, v136
	v_pk_mul_f16 v149, v44, v137
	v_pk_mul_f16 v150, v49, v136
	v_pk_mul_f16 v151, v45, v137
	v_mfma_f32_32x32x16_f16 a[208:223], v[38:41], v[122:125], a[208:223]
	ds_read_b128 v[66:69], v147 offset:18464
	v_pk_max_f16 v148, v148, v149
	v_pk_max_f16 v150, v150, v151
	v_cndmask_b32_e64 v149, v1, v148, s[44:45]
	v_cndmask_b32_e64 v148, v1, v148, s[46:47]
	v_mfma_f32_32x32x16_f16 a[48:63], v[18:21], v[118:121], a[48:63]
	ds_read_b128 v[70:73], v147 offset:23072
	v_perm_b32 v116, v148, v149, s33
	v_cndmask_b32_e64 v151, v1, v150, s[48:49]
	v_cndmask_b32_e64 v150, v1, v150, s[50:51]
	v_perm_b32 v117, v150, v151, s33
	v_mfma_f32_32x32x16_f16 a[192:207], v[38:41], v[118:121], a[192:207]
	ds_read_b128 v[78:81], v147 offset:27680
	v_pk_add_f16 v148, v115, v114
	v_pk_add_f16 v149, v116, v117
	v_pk_mul_f16 v152, v46, v140
	v_pk_add_f16 v148, v148, v149
	v_mfma_f32_32x32x16_f16 a[64:79], v[18:21], v[106:109], a[64:79]
	ds_read_b128 v[102:105], v147 offset:32288
	v_pk_mul_f16 v153, v42, v139
	v_dot2c_f32_f16_e32 v134, 0x3c003c00, v148
	v_pk_mul_f16 v154, v47, v140
	v_pk_mul_f16 v155, v43, v139
	v_mfma_f32_32x32x16_f16 a[176:191], v[38:41], v[106:109], a[176:191]
	v_pk_max_f16 v152, v152, v153
	v_pk_max_f16 v154, v154, v155
	v_cndmask_b32_e64 v153, v138, v152, s[4:5]
	v_cndmask_b32_e64 v152, v138, v152, s[6:7]
	v_mfma_f32_32x32x16_f16 a[112:127], v[18:21], v[98:101], a[112:127]
	v_perm_b32 v110, v152, v153, s33
	v_cndmask_b32_e64 v155, v138, v154, s[8:9]
	v_cndmask_b32_e64 v154, v138, v154, s[10:11]
	v_perm_b32 v111, v154, v155, s33
	v_mfma_f32_32x32x16_f16 a[160:175], v[38:41], v[98:101], a[160:175]
	v_pk_mul_f16 v152, v48, v140
	v_pk_mul_f16 v153, v44, v139
	v_pk_mul_f16 v154, v49, v140
	v_pk_mul_f16 v155, v45, v139
	v_pk_max_f16 v152, v152, v153
	v_mfma_f32_32x32x16_f16 a[128:143], v[18:21], v[94:97], a[128:143]
	v_pk_max_f16 v154, v154, v155
	v_cndmask_b32_e64 v153, v138, v152, s[12:13]
	v_cndmask_b32_e64 v152, v138, v152, s[14:15]
	v_perm_b32 v112, v152, v153, s33
	v_cndmask_b32_e64 v155, v138, v154, s[16:17]
	v_mfma_f32_32x32x16_f16 a[144:159], v[38:41], v[94:97], a[144:159]
	v_cndmask_b32_e64 v154, v138, v154, s[18:19]
	v_perm_b32 v113, v154, v155, s33
	v_pk_add_f16 v152, v111, v110
	v_pk_add_f16 v153, v112, v113
	v_mfma_f32_32x32x16_f16 a[80:95], v[18:21], v[86:89], a[80:95]
	v_pk_add_f16 v152, v152, v153
	v_mfma_f32_32x32x16_f16 a[96:111], v[38:41], v[86:89], a[96:111]
	v_dot2c_f32_f16_e32 v135, 0x3c003c00, v152
	s_waitcnt lgkmcnt(0)
	v_mfma_f32_32x32x16_f16 a[0:15], v[114:117], v[50:53], a[0:15]
	s_load_dwordx16 s[36:51], s[30:31], 0xc0
	s_load_dwordx16 s[4:19], s[30:31], 0x80c0
	ds_read_b128 v[46:49], v145 offset:32
	ds_read_b128 v[42:45], v145 offset:2080
	v_mfma_f32_32x32x16_f16 a[240:255], v[110:113], v[50:53], a[240:255]
	ds_read_b128 v[74:77], v147 offset:64
	v_pk_mul_f16 v148, v90, v136
	v_pk_mul_f16 v149, v82, v137
	v_pk_mul_f16 v150, v91, v136
	v_pk_mul_f16 v151, v83, v137
	v_mfma_f32_32x32x16_f16 a[16:31], v[114:117], v[54:57], a[16:31]
	ds_read_b128 v[126:129], v147 offset:4672
	v_pk_max_f16 v148, v148, v149
	v_pk_max_f16 v150, v150, v151
	v_cndmask_b32_e64 v149, v1, v148, s[68:69]
	v_cndmask_b32_e64 v148, v1, v148, s[70:71]
	v_mfma_f32_32x32x16_f16 a[224:239], v[110:113], v[54:57], a[224:239]
	ds_read_b128 v[122:125], v147 offset:9280
	v_perm_b32 v18, v148, v149, s33
	v_cndmask_b32_e64 v151, v1, v150, s[72:73]
	v_cndmask_b32_e64 v150, v1, v150, s[74:75]
	v_perm_b32 v19, v150, v151, s33
	v_mfma_f32_32x32x16_f16 a[32:47], v[114:117], v[58:61], a[32:47]
	ds_read_b128 v[118:121], v147 offset:13888
	v_pk_mul_f16 v148, v92, v136
	v_pk_mul_f16 v149, v84, v137
	v_pk_mul_f16 v150, v93, v136
	v_pk_mul_f16 v151, v85, v137
	v_mfma_f32_32x32x16_f16 a[208:223], v[110:113], v[58:61], a[208:223]
	ds_read_b128 v[106:109], v147 offset:18496
	v_pk_max_f16 v148, v148, v149
	v_pk_max_f16 v150, v150, v151
	v_cndmask_b32_e64 v149, v1, v148, s[76:77]
	v_cndmask_b32_e64 v148, v1, v148, s[78:79]
	v_mfma_f32_32x32x16_f16 a[48:63], v[114:117], v[62:65], a[48:63]
	ds_read_b128 v[98:101], v147 offset:23104
	v_perm_b32 v20, v148, v149, s33
	v_cndmask_b32_e64 v151, v1, v150, s[80:81]
	v_cndmask_b32_e64 v150, v1, v150, s[82:83]
	v_perm_b32 v21, v150, v151, s33
	v_mfma_f32_32x32x16_f16 a[192:207], v[110:113], v[62:65], a[192:207]
	ds_read_b128 v[94:97], v147 offset:27712
	v_pk_add_f16 v148, v19, v18
	v_pk_add_f16 v149, v20, v21
	v_pk_mul_f16 v152, v90, v140
	v_pk_add_f16 v148, v148, v149
	v_mfma_f32_32x32x16_f16 a[64:79], v[114:117], v[66:69], a[64:79]
	ds_read_b128 v[86:89], v147 offset:32320
	v_pk_mul_f16 v153, v82, v139
	v_dot2c_f32_f16_e32 v134, 0x3c003c00, v148
	v_pk_mul_f16 v154, v91, v140
	v_pk_mul_f16 v155, v83, v139
	v_mfma_f32_32x32x16_f16 a[176:191], v[110:113], v[66:69], a[176:191]
	v_pk_max_f16 v152, v152, v153
	v_pk_max_f16 v154, v154, v155
	v_cndmask_b32_e64 v153, v138, v152, s[52:53]
	v_cndmask_b32_e64 v152, v138, v152, s[54:55]
	v_mfma_f32_32x32x16_f16 a[112:127], v[114:117], v[70:73], a[112:127]
	v_perm_b32 v38, v152, v153, s33
	v_cndmask_b32_e64 v155, v138, v154, s[56:57]
	v_cndmask_b32_e64 v154, v138, v154, s[58:59]
	v_perm_b32 v39, v154, v155, s33
	v_mfma_f32_32x32x16_f16 a[160:175], v[110:113], v[70:73], a[160:175]
	v_pk_mul_f16 v152, v92, v140
	v_pk_mul_f16 v153, v84, v139
	v_pk_mul_f16 v154, v93, v140
	v_pk_mul_f16 v155, v85, v139
	v_pk_max_f16 v152, v152, v153
	v_mfma_f32_32x32x16_f16 a[128:143], v[114:117], v[78:81], a[128:143]
	v_pk_max_f16 v154, v154, v155
	v_cndmask_b32_e64 v153, v138, v152, s[60:61]
	v_cndmask_b32_e64 v152, v138, v152, s[62:63]
	v_perm_b32 v40, v152, v153, s33
	v_cndmask_b32_e64 v155, v138, v154, s[64:65]
	v_mfma_f32_32x32x16_f16 a[144:159], v[110:113], v[78:81], a[144:159]
	v_cndmask_b32_e64 v154, v138, v154, s[66:67]
	v_perm_b32 v41, v154, v155, s33
	v_pk_add_f16 v152, v39, v38
	v_pk_add_f16 v153, v40, v41
	v_mfma_f32_32x32x16_f16 a[80:95], v[114:117], v[102:105], a[80:95]
	v_pk_add_f16 v152, v152, v153
	v_mfma_f32_32x32x16_f16 a[96:111], v[110:113], v[102:105], a[96:111]
	v_dot2c_f32_f16_e32 v135, 0x3c003c00, v152
	s_waitcnt lgkmcnt(0)
	v_mfma_f32_32x32x16_f16 a[0:15], v[18:21], v[74:77], a[0:15]
	s_load_dwordx16 s[68:83], s[30:31], 0x100
	s_load_dwordx16 s[52:67], s[30:31], 0x8100
	ds_read_b128 v[90:93], v145 offset:64
	ds_read_b128 v[82:85], v145 offset:2112
	v_mfma_f32_32x32x16_f16 a[240:255], v[38:41], v[74:77], a[240:255]
	ds_read_b128 v[50:53], v147 offset:96
	v_pk_mul_f16 v148, v46, v136
	v_pk_mul_f16 v149, v42, v137
	v_pk_mul_f16 v150, v47, v136
	v_pk_mul_f16 v151, v43, v137
	v_mfma_f32_32x32x16_f16 a[16:31], v[18:21], v[126:129], a[16:31]
	ds_read_b128 v[54:57], v147 offset:4704
	v_pk_max_f16 v148, v148, v149
	v_pk_max_f16 v150, v150, v151
	v_cndmask_b32_e64 v149, v1, v148, s[36:37]
	v_cndmask_b32_e64 v148, v1, v148, s[38:39]
	v_mfma_f32_32x32x16_f16 a[224:239], v[38:41], v[126:129], a[224:239]
	ds_read_b128 v[58:61], v147 offset:9312
	v_perm_b32 v114, v148, v149, s33
	v_cndmask_b32_e64 v151, v1, v150, s[40:41]
	v_cndmask_b32_e64 v150, v1, v150, s[42:43]
	v_perm_b32 v115, v150, v151, s33
	v_mfma_f32_32x32x16_f16 a[32:47], v[18:21], v[122:125], a[32:47]
	ds_read_b128 v[62:65], v147 offset:13920
	v_pk_mul_f16 v148, v48, v136
	v_pk_mul_f16 v149, v44, v137
	v_pk_mul_f16 v150, v49, v136
	v_pk_mul_f16 v151, v45, v137
	v_mfma_f32_32x32x16_f16 a[208:223], v[38:41], v[122:125], a[208:223]
	ds_read_b128 v[66:69], v147 offset:18528
	v_pk_max_f16 v148, v148, v149
	v_pk_max_f16 v150, v150, v151
	v_cndmask_b32_e64 v149, v1, v148, s[44:45]
	v_cndmask_b32_e64 v148, v1, v148, s[46:47]
	v_mfma_f32_32x32x16_f16 a[48:63], v[18:21], v[118:121], a[48:63]
	ds_read_b128 v[70:73], v147 offset:23136
	v_perm_b32 v116, v148, v149, s33
	v_cndmask_b32_e64 v151, v1, v150, s[48:49]
	v_cndmask_b32_e64 v150, v1, v150, s[50:51]
	v_perm_b32 v117, v150, v151, s33
	v_mfma_f32_32x32x16_f16 a[192:207], v[38:41], v[118:121], a[192:207]
	ds_read_b128 v[78:81], v147 offset:27744
	v_pk_add_f16 v148, v115, v114
	v_pk_add_f16 v149, v116, v117
	v_pk_mul_f16 v152, v46, v140
	v_pk_add_f16 v148, v148, v149
	v_mfma_f32_32x32x16_f16 a[64:79], v[18:21], v[106:109], a[64:79]
	ds_read_b128 v[102:105], v147 offset:32352
	v_pk_mul_f16 v153, v42, v139
	v_dot2c_f32_f16_e32 v134, 0x3c003c00, v148
	v_pk_mul_f16 v154, v47, v140
	v_pk_mul_f16 v155, v43, v139
	v_mfma_f32_32x32x16_f16 a[176:191], v[38:41], v[106:109], a[176:191]
	v_pk_max_f16 v152, v152, v153
	v_pk_max_f16 v154, v154, v155
	v_cndmask_b32_e64 v153, v138, v152, s[4:5]
	v_cndmask_b32_e64 v152, v138, v152, s[6:7]
	v_mfma_f32_32x32x16_f16 a[112:127], v[18:21], v[98:101], a[112:127]
	v_perm_b32 v110, v152, v153, s33
	v_cndmask_b32_e64 v155, v138, v154, s[8:9]
	v_cndmask_b32_e64 v154, v138, v154, s[10:11]
	v_perm_b32 v111, v154, v155, s33
	v_mfma_f32_32x32x16_f16 a[160:175], v[38:41], v[98:101], a[160:175]
	v_pk_mul_f16 v152, v48, v140
	v_pk_mul_f16 v153, v44, v139
	v_pk_mul_f16 v154, v49, v140
	v_pk_mul_f16 v155, v45, v139
	v_pk_max_f16 v152, v152, v153
	v_mfma_f32_32x32x16_f16 a[128:143], v[18:21], v[94:97], a[128:143]
	v_pk_max_f16 v154, v154, v155
	v_cndmask_b32_e64 v153, v138, v152, s[12:13]
	v_cndmask_b32_e64 v152, v138, v152, s[14:15]
	v_perm_b32 v112, v152, v153, s33
	v_cndmask_b32_e64 v155, v138, v154, s[16:17]
	v_mfma_f32_32x32x16_f16 a[144:159], v[38:41], v[94:97], a[144:159]
	v_cndmask_b32_e64 v154, v138, v154, s[18:19]
	v_perm_b32 v113, v154, v155, s33
	v_pk_add_f16 v152, v111, v110
	v_pk_add_f16 v153, v112, v113
	v_mfma_f32_32x32x16_f16 a[80:95], v[18:21], v[86:89], a[80:95]
	v_pk_add_f16 v152, v152, v153
	v_mfma_f32_32x32x16_f16 a[96:111], v[38:41], v[86:89], a[96:111]
	v_dot2c_f32_f16_e32 v135, 0x3c003c00, v152
	s_waitcnt lgkmcnt(0)
	v_mfma_f32_32x32x16_f16 a[0:15], v[114:117], v[50:53], a[0:15]
	s_load_dwordx16 s[36:51], s[30:31], 0x140
	s_load_dwordx16 s[4:19], s[30:31], 0x8140
	ds_read_b128 v[46:49], v145 offset:96
	ds_read_b128 v[42:45], v145 offset:2144
	v_mfma_f32_32x32x16_f16 a[240:255], v[110:113], v[50:53], a[240:255]
	ds_read_b128 v[74:77], v146
	v_pk_mul_f16 v148, v90, v136
	v_pk_mul_f16 v149, v82, v137
	v_pk_mul_f16 v150, v91, v136
	v_pk_mul_f16 v151, v83, v137
	v_mfma_f32_32x32x16_f16 a[16:31], v[114:117], v[54:57], a[16:31]
	ds_read_b128 v[126:129], v146 offset:4608
	v_pk_max_f16 v148, v148, v149
	v_pk_max_f16 v150, v150, v151
	v_cndmask_b32_e64 v149, v1, v148, s[68:69]
	v_cndmask_b32_e64 v148, v1, v148, s[70:71]
	v_mfma_f32_32x32x16_f16 a[224:239], v[110:113], v[54:57], a[224:239]
	ds_read_b128 v[122:125], v146 offset:9216
	v_perm_b32 v18, v148, v149, s33
	v_cndmask_b32_e64 v151, v1, v150, s[72:73]
	v_cndmask_b32_e64 v150, v1, v150, s[74:75]
	v_perm_b32 v19, v150, v151, s33
	v_mfma_f32_32x32x16_f16 a[32:47], v[114:117], v[58:61], a[32:47]
	ds_read_b128 v[118:121], v146 offset:13824
	v_pk_mul_f16 v148, v92, v136
	v_pk_mul_f16 v149, v84, v137
	v_pk_mul_f16 v150, v93, v136
	v_pk_mul_f16 v151, v85, v137
	v_mfma_f32_32x32x16_f16 a[208:223], v[110:113], v[58:61], a[208:223]
	ds_read_b128 v[106:109], v146 offset:18432
	v_pk_max_f16 v148, v148, v149
	v_pk_max_f16 v150, v150, v151
	v_cndmask_b32_e64 v149, v1, v148, s[76:77]
	v_cndmask_b32_e64 v148, v1, v148, s[78:79]
	v_mfma_f32_32x32x16_f16 a[48:63], v[114:117], v[62:65], a[48:63]
	ds_read_b128 v[98:101], v146 offset:23040
	v_perm_b32 v20, v148, v149, s33
	v_cndmask_b32_e64 v151, v1, v150, s[80:81]
	v_cndmask_b32_e64 v150, v1, v150, s[82:83]
	v_perm_b32 v21, v150, v151, s33
	v_mfma_f32_32x32x16_f16 a[192:207], v[110:113], v[62:65], a[192:207]
	ds_read_b128 v[94:97], v146 offset:27648
	v_pk_add_f16 v148, v19, v18
	v_pk_add_f16 v149, v20, v21
	v_pk_mul_f16 v152, v90, v140
	v_pk_add_f16 v148, v148, v149
	v_mfma_f32_32x32x16_f16 a[64:79], v[114:117], v[66:69], a[64:79]
	ds_read_b128 v[86:89], v146 offset:32256
	v_pk_mul_f16 v153, v82, v139
	v_dot2c_f32_f16_e32 v134, 0x3c003c00, v148
	v_pk_mul_f16 v154, v91, v140
	v_pk_mul_f16 v155, v83, v139
	v_mfma_f32_32x32x16_f16 a[176:191], v[110:113], v[66:69], a[176:191]
	v_pk_max_f16 v152, v152, v153
	v_pk_max_f16 v154, v154, v155
	v_cndmask_b32_e64 v153, v138, v152, s[52:53]
	v_cndmask_b32_e64 v152, v138, v152, s[54:55]
	v_mfma_f32_32x32x16_f16 a[112:127], v[114:117], v[70:73], a[112:127]
	v_perm_b32 v38, v152, v153, s33
	v_cndmask_b32_e64 v155, v138, v154, s[56:57]
	v_cndmask_b32_e64 v154, v138, v154, s[58:59]
	v_perm_b32 v39, v154, v155, s33
	v_mfma_f32_32x32x16_f16 a[160:175], v[110:113], v[70:73], a[160:175]
	v_pk_mul_f16 v152, v92, v140
	v_pk_mul_f16 v153, v84, v139
	v_pk_mul_f16 v154, v93, v140
	v_pk_mul_f16 v155, v85, v139
	v_pk_max_f16 v152, v152, v153
	v_mfma_f32_32x32x16_f16 a[128:143], v[114:117], v[78:81], a[128:143]
	v_pk_max_f16 v154, v154, v155
	v_cndmask_b32_e64 v153, v138, v152, s[60:61]
	v_cndmask_b32_e64 v152, v138, v152, s[62:63]
	v_perm_b32 v40, v152, v153, s33
	v_cndmask_b32_e64 v155, v138, v154, s[64:65]
	v_mfma_f32_32x32x16_f16 a[144:159], v[110:113], v[78:81], a[144:159]
	v_cndmask_b32_e64 v154, v138, v154, s[66:67]
	v_perm_b32 v41, v154, v155, s33
	v_pk_add_f16 v152, v39, v38
	v_pk_add_f16 v153, v40, v41
	v_mfma_f32_32x32x16_f16 a[80:95], v[114:117], v[102:105], a[80:95]
	v_pk_add_f16 v152, v152, v153
	v_mfma_f32_32x32x16_f16 a[96:111], v[110:113], v[102:105], a[96:111]
	v_dot2c_f32_f16_e32 v135, 0x3c003c00, v152
	s_add_i32 s92, s92, 0x9000
	s_cmp_lg_u32 s91, 2
	s_cselect_b32 s30, s92, 0
	s_add_u32 s20, s20, 0x100
	s_addc_u32 s21, s21, 0
	v_add_u32_e32 v50, s30, v144
	v_lshl_add_u64 v[130:131], v[130:131], 0, s[28:29]
	v_add_u32_e32 v145, 0x80, v145
	s_cmpk_eq_i32 s20, 0xf00
	s_mov_b32 s30, s91
	s_waitcnt vmcnt(6)
	s_waitcnt vmcnt(5)
	s_waitcnt vmcnt(4)
	s_waitcnt vmcnt(3)
	s_waitcnt vmcnt(2)
	s_waitcnt vmcnt(1)
	s_waitcnt vmcnt(0)
	ds_write_b128 v50, v[6:9]
	ds_write_b128 v50, v[2:5] offset:4608
	ds_write_b128 v50, v[14:17] offset:9216
	ds_write_b128 v50, v[10:13] offset:13824
	ds_write_b128 v50, v[26:29] offset:18432
	ds_write_b128 v50, v[22:25] offset:23040
	ds_write_b128 v50, v[30:33] offset:27648
	ds_write_b128 v50, v[34:37] offset:32256
	s_waitcnt lgkmcnt(0)
	s_barrier
	s_cbranch_scc0 .LBB1_3
	v_accvgpr_read_b32 v175, a95
	v_accvgpr_read_b32 v174, a94
	v_accvgpr_read_b32 v173, a93
	v_accvgpr_read_b32 v172, a92
	v_accvgpr_read_b32 v171, a91
	v_accvgpr_read_b32 v170, a90
	v_accvgpr_read_b32 v169, a89
	v_accvgpr_read_b32 v168, a88
	v_accvgpr_read_b32 v167, a87
	v_accvgpr_read_b32 v166, a86
	v_accvgpr_read_b32 v165, a85
	v_accvgpr_read_b32 v164, a84
	v_accvgpr_read_b32 v163, a83
	v_accvgpr_read_b32 v162, a82
	v_accvgpr_read_b32 v161, a81
	v_accvgpr_read_b32 v160, a80
	v_mfma_f32_32x32x16_f16 a[80:95], v[18:21], v[74:77], a[0:15]
	s_nop 11
	v_accvgpr_read_b32 v159, a95
	v_accvgpr_read_b32 v158, a94
	v_accvgpr_read_b32 v157, a93
	v_accvgpr_read_b32 v156, a92
	v_accvgpr_read_b32 v155, a91
	v_accvgpr_read_b32 v154, a90
	v_accvgpr_read_b32 v153, a89
	v_accvgpr_read_b32 v152, a88
	v_accvgpr_read_b32 v151, a87
	v_accvgpr_read_b32 v150, a86
	v_accvgpr_read_b32 v149, a85
	v_accvgpr_read_b32 v148, a84
	v_accvgpr_read_b32 v147, a83
	v_accvgpr_read_b32 v146, a82
	v_accvgpr_read_b32 v145, a81
	v_accvgpr_read_b32 v144, a80
	ds_read_b128 v[2:5], v141 offset:32288
	ds_read_b128 v[82:85], v141 offset:32
	ds_read_b128 v[58:61], v141 offset:4640
	ds_read_b128 v[50:53], v141 offset:9248
	ds_read_b128 v[26:29], v141 offset:13856
	ds_read_b128 v[22:25], v141 offset:18464
	ds_read_b128 v[14:17], v141 offset:23072
	ds_read_b128 v[10:13], v141 offset:27680
	s_load_dwordx16 s[68:83], s[0:1], 0xf80
	s_load_dwordx16 s[52:67], s[0:1], 0x8f80
	ds_read_b128 v[54:57], v142 offset:1984
	ds_read_b128 v[34:37], v143 offset:1984
	v_mfma_f32_32x32x16_f16 a[0:15], v[38:41], v[74:77], a[240:255]
	v_pk_mul_f16 v6, v46, v136
	v_pk_mul_f16 v7, v42, v137
	s_mov_b32 s20, 0x7060100
	v_pk_max_f16 v6, v6, v7
	s_nop 0
	v_cndmask_b32_e64 v7, v1, v6, s[36:37]
	v_mfma_f32_32x32x16_f16 a[240:255], v[18:21], v[126:129], a[16:31]
	v_cndmask_b32_e64 v6, v1, v6, s[38:39]
	v_perm_b32 v74, v6, v7, s20
	v_pk_mul_f16 v6, v47, v136
	v_pk_mul_f16 v7, v43, v137
	v_mfma_f32_32x32x16_f16 a[16:31], v[38:41], v[126:129], a[224:239]
	v_pk_max_f16 v6, v6, v7
	s_nop 0
	v_cndmask_b32_e64 v7, v1, v6, s[40:41]
	v_cndmask_b32_e64 v6, v1, v6, s[42:43]
	v_perm_b32 v75, v6, v7, s20
	v_mfma_f32_32x32x16_f16 a[224:239], v[18:21], v[122:125], a[32:47]
	v_pk_mul_f16 v6, v48, v136
	v_pk_mul_f16 v7, v44, v137
	s_nop 0
	v_pk_max_f16 v6, v6, v7
	s_nop 0
	v_cndmask_b32_e64 v7, v1, v6, s[44:45]
	v_mfma_f32_32x32x16_f16 a[32:47], v[38:41], v[122:125], a[208:223]
	v_cndmask_b32_e64 v6, v1, v6, s[46:47]
	v_perm_b32 v76, v6, v7, s20
	v_pk_mul_f16 v6, v49, v136
	v_pk_mul_f16 v7, v45, v137
	v_mfma_f32_32x32x16_f16 a[208:223], v[18:21], v[118:121], a[48:63]
	v_pk_max_f16 v6, v6, v7
	s_nop 0
	v_cndmask_b32_e64 v7, v1, v6, s[48:49]
	v_cndmask_b32_e64 v6, v1, v6, s[50:51]
	v_perm_b32 v77, v6, v7, s20
	v_mfma_f32_32x32x16_f16 a[48:63], v[38:41], v[118:121], a[192:207]
	v_pk_add_f16 v6, v75, v74
	v_pk_add_f16 v7, v76, v77
	s_nop 0
	v_pk_add_f16 v6, v6, v7
	s_nop 0
	v_dot2c_f32_f16_e32 v134, 0x3c003c00, v6
	v_mfma_f32_32x32x16_f16 a[192:207], v[18:21], v[106:109], a[64:79]
	v_pk_mul_f16 v6, v46, v140
	v_pk_mul_f16 v7, v42, v139
	s_nop 0
	v_pk_max_f16 v6, v6, v7
	s_nop 0
	v_cndmask_b32_e64 v7, v138, v6, s[4:5]
	v_mfma_f32_32x32x16_f16 a[64:79], v[38:41], v[106:109], a[176:191]
	v_pk_mul_f16 v8, v47, v140
	v_pk_mul_f16 v9, v43, v139
	v_cndmask_b32_e64 v6, v138, v6, s[6:7]
	v_pk_max_f16 v8, v8, v9
	v_mfma_f32_32x32x16_f16 a[176:191], v[18:21], v[98:101], a[112:127]
	v_pk_mul_f16 v30, v48, v140
	v_pk_mul_f16 v31, v44, v139
	v_cndmask_b32_e64 v9, v138, v8, s[8:9]
	v_cndmask_b32_e64 v8, v138, v8, s[10:11]
	v_mfma_f32_32x32x16_f16 a[112:127], v[38:41], v[98:101], a[160:175]
	v_pk_max_f16 v30, v30, v31
	v_pk_mul_f16 v32, v49, v140
	v_cndmask_b32_e64 v31, v138, v30, s[12:13]
	v_cndmask_b32_e64 v30, v138, v30, s[14:15]
	v_mfma_f32_32x32x16_f16 a[160:175], v[18:21], v[94:97], a[128:143]
	v_pk_mul_f16 v33, v45, v139
	s_nop 0
	v_pk_max_f16 v32, v32, v33
	s_nop 0
	v_cndmask_b32_e64 v33, v138, v32, s[16:17]
	v_cndmask_b32_e64 v32, v138, v32, s[18:19]
	v_mfma_f32_32x32x16_f16 a[128:143], v[38:41], v[94:97], a[144:159]
	v_perm_b32 v78, v6, v7, s20
	v_perm_b32 v79, v8, v9, s20
	v_perm_b32 v80, v30, v31, s20
	v_perm_b32 v81, v32, v33, s20
	v_pk_add_f16 v6, v79, v78
	v_pk_add_f16 v7, v80, v81
	v_accvgpr_write_b32 a80, v160
	v_pk_add_f16 v6, v6, v7
	v_accvgpr_write_b32 a81, v161
	v_accvgpr_write_b32 a82, v162
	v_accvgpr_write_b32 a83, v163
	v_accvgpr_write_b32 a84, v164
	v_accvgpr_write_b32 a85, v165
	v_accvgpr_write_b32 a86, v166
	v_accvgpr_write_b32 a87, v167
	v_accvgpr_write_b32 a88, v168
	v_accvgpr_write_b32 a89, v169
	v_accvgpr_write_b32 a90, v170
	v_accvgpr_write_b32 a91, v171
	v_accvgpr_write_b32 a92, v172
	v_accvgpr_write_b32 a93, v173
	v_accvgpr_write_b32 a94, v174
	v_accvgpr_write_b32 a95, v175
	v_dot2c_f32_f16_e32 v135, 0x3c003c00, v6
	s_nop 0
	v_mfma_f32_32x32x16_f16 a[144:159], v[18:21], v[86:89], a[80:95]
	v_mfma_f32_32x32x16_f16 a[80:95], v[38:41], v[86:89], a[96:111]
	s_nop 6
	v_accvgpr_write_b32 a96, v144
	v_accvgpr_write_b32 a97, v145
	v_accvgpr_write_b32 a98, v146
	v_accvgpr_write_b32 a99, v147
	v_accvgpr_write_b32 a100, v148
	v_accvgpr_write_b32 a101, v149
	v_accvgpr_write_b32 a102, v150
	v_accvgpr_write_b32 a103, v151
	v_accvgpr_write_b32 a104, v152
	v_accvgpr_write_b32 a105, v153
	v_accvgpr_write_b32 a106, v154
	v_accvgpr_write_b32 a107, v155
	v_accvgpr_write_b32 a108, v156
	v_accvgpr_write_b32 a109, v157
	v_accvgpr_write_b32 a110, v158
	v_accvgpr_write_b32 a111, v159
	s_waitcnt lgkmcnt(0)
	s_nop 0
	v_mfma_f32_32x32x16_f16 a[96:111], v[74:77], v[82:85], a[96:111]
	ds_read_b128 v[86:89], v141 offset:64
	ds_read_b128 v[70:73], v141 offset:4672
	ds_read_b128 v[62:65], v141 offset:9280
	ds_read_b128 v[42:45], v141 offset:13888
	ds_read_b128 v[38:41], v141 offset:18496
	ds_read_b128 v[30:33], v141 offset:23104
	ds_read_b128 v[18:21], v141 offset:27712
	ds_read_b128 v[6:9], v141 offset:32320
	s_load_dwordx16 s[36:51], s[0:1], 0xfc0
	s_load_dwordx16 s[4:19], s[0:1], 0x8fc0
	ds_read_b128 v[66:69], v142 offset:2016
	ds_read_b128 v[46:49], v143 offset:2016
	v_mfma_f32_32x32x16_f16 a[0:15], v[78:81], v[82:85], a[0:15]
	v_pk_mul_f16 v82, v54, v136
	v_pk_mul_f16 v83, v34, v137
	s_nop 0
	v_pk_max_f16 v82, v82, v83
	s_nop 0
	v_cndmask_b32_e64 v83, v1, v82, s[68:69]
	v_mfma_f32_32x32x16_f16 a[240:255], v[74:77], v[58:61], a[240:255]
	v_cndmask_b32_e64 v82, v1, v82, s[70:71]
	v_perm_b32 v82, v82, v83, s20
	v_pk_mul_f16 v83, v55, v136
	v_pk_mul_f16 v84, v35, v137
	v_mfma_f32_32x32x16_f16 a[16:31], v[78:81], v[58:61], a[16:31]
	v_pk_max_f16 v58, v83, v84
	s_nop 0
	v_cndmask_b32_e64 v59, v1, v58, s[72:73]
	v_cndmask_b32_e64 v58, v1, v58, s[74:75]
	v_perm_b32 v83, v58, v59, s20
	v_mfma_f32_32x32x16_f16 a[224:239], v[74:77], v[50:53], a[224:239]
	v_pk_mul_f16 v58, v56, v136
	v_pk_mul_f16 v59, v36, v137
	s_nop 0
	v_pk_max_f16 v58, v58, v59
	s_nop 0
	v_cndmask_b32_e64 v59, v1, v58, s[76:77]
	v_mfma_f32_32x32x16_f16 a[32:47], v[78:81], v[50:53], a[32:47]
	v_cndmask_b32_e64 v50, v1, v58, s[78:79]
	v_perm_b32 v84, v50, v59, s20
	v_pk_mul_f16 v50, v57, v136
	v_pk_mul_f16 v51, v37, v137
	v_mfma_f32_32x32x16_f16 a[208:223], v[74:77], v[26:29], a[208:223]
	v_pk_max_f16 v50, v50, v51
	s_nop 0
	v_cndmask_b32_e64 v51, v1, v50, s[80:81]
	v_cndmask_b32_e64 v50, v1, v50, s[82:83]
	v_perm_b32 v85, v50, v51, s20
	v_mfma_f32_32x32x16_f16 a[48:63], v[78:81], v[26:29], a[48:63]
	v_pk_add_f16 v26, v83, v82
	v_pk_add_f16 v27, v84, v85
	s_nop 0
	v_pk_add_f16 v26, v26, v27
	s_nop 0
	v_dot2c_f32_f16_e32 v134, 0x3c003c00, v26
	v_mfma_f32_32x32x16_f16 a[192:207], v[74:77], v[22:25], a[192:207]
	v_pk_mul_f16 v26, v54, v140
	v_pk_mul_f16 v27, v34, v139
	s_nop 0
	v_pk_max_f16 v26, v26, v27
	s_nop 0
	v_cndmask_b32_e64 v27, v138, v26, s[52:53]
	v_mfma_f32_32x32x16_f16 a[64:79], v[78:81], v[22:25], a[64:79]
	v_pk_mul_f16 v23, v55, v140
	v_pk_mul_f16 v24, v35, v139
	v_cndmask_b32_e64 v22, v138, v26, s[54:55]
	v_pk_max_f16 v23, v23, v24
	v_mfma_f32_32x32x16_f16 a[176:191], v[74:77], v[14:17], a[176:191]
	v_pk_mul_f16 v25, v56, v140
	v_pk_mul_f16 v26, v36, v139
	v_cndmask_b32_e64 v24, v138, v23, s[56:57]
	v_cndmask_b32_e64 v23, v138, v23, s[58:59]
	v_mfma_f32_32x32x16_f16 a[112:127], v[78:81], v[14:17], a[112:127]
	v_pk_max_f16 v14, v25, v26
	v_pk_mul_f16 v16, v57, v140
	v_cndmask_b32_e64 v15, v138, v14, s[60:61]
	v_cndmask_b32_e64 v14, v138, v14, s[62:63]
	v_mfma_f32_32x32x16_f16 a[160:175], v[74:77], v[10:13], a[160:175]
	v_pk_mul_f16 v17, v37, v139
	s_nop 0
	v_pk_max_f16 v16, v16, v17
	s_nop 0
	v_cndmask_b32_e64 v17, v138, v16, s[64:65]
	v_cndmask_b32_e64 v16, v138, v16, s[66:67]
	v_mfma_f32_32x32x16_f16 a[128:143], v[78:81], v[10:13], a[128:143]
	v_perm_b32 v10, v22, v27, s20
	v_perm_b32 v11, v23, v24, s20
	v_perm_b32 v12, v14, v15, s20
	v_perm_b32 v13, v16, v17, s20
	v_mfma_f32_32x32x16_f16 a[144:159], v[74:77], v[2:5], a[144:159]
	v_pk_add_f16 v14, v11, v10
	v_pk_add_f16 v15, v12, v13
	s_nop 0
	v_pk_add_f16 v14, v14, v15
	s_nop 0
	v_dot2c_f32_f16_e32 v135, 0x3c003c00, v14
	v_mfma_f32_32x32x16_f16 a[80:95], v[78:81], v[2:5], a[80:95]
	s_waitcnt lgkmcnt(0)
	v_mfma_f32_32x32x16_f16 a[96:111], v[82:85], v[86:89], a[96:111]
	ds_read_b128 v[2:5], v141 offset:96
	ds_read_b128 v[14:17], v141 offset:4704
	ds_read_b128 v[22:25], v141 offset:9312
	ds_read_b128 v[26:29], v141 offset:13920
	ds_read_b128 v[34:37], v141 offset:18528
	ds_read_b128 v[50:53], v141 offset:23136
	ds_read_b128 v[54:57], v141 offset:27744
	ds_read_b128 v[58:61], v141 offset:32352
	v_mfma_f32_32x32x16_f16 a[0:15], v[10:13], v[86:89], a[0:15]
	v_pk_mul_f16 v74, v136, v66
	v_pk_mul_f16 v75, v137, v46
	s_nop 0
	v_pk_max_f16 v74, v74, v75
	s_nop 0
	v_cndmask_b32_e64 v75, v1, v74, s[36:37]
	v_mfma_f32_32x32x16_f16 a[240:255], v[82:85], v[70:73], a[240:255]
	v_cndmask_b32_e64 v74, v1, v74, s[38:39]
	v_perm_b32 v74, v74, v75, s20
	v_pk_mul_f16 v75, v136, v67
	v_pk_mul_f16 v76, v137, v47
	v_mfma_f32_32x32x16_f16 a[16:31], v[10:13], v[70:73], a[16:31]
	v_pk_max_f16 v70, v75, v76
	s_nop 0
	v_cndmask_b32_e64 v71, v1, v70, s[40:41]
	v_cndmask_b32_e64 v70, v1, v70, s[42:43]
	v_perm_b32 v75, v70, v71, s20
	v_mfma_f32_32x32x16_f16 a[224:239], v[82:85], v[62:65], a[224:239]
	v_pk_mul_f16 v70, v136, v68
	v_pk_mul_f16 v71, v137, v48
	s_nop 0
	v_pk_max_f16 v70, v70, v71
	s_nop 0
	v_cndmask_b32_e64 v71, v1, v70, s[44:45]
	v_mfma_f32_32x32x16_f16 a[32:47], v[10:13], v[62:65], a[32:47]
	v_cndmask_b32_e64 v62, v1, v70, s[46:47]
	v_perm_b32 v76, v62, v71, s20
	v_pk_mul_f16 v62, v136, v69
	v_pk_mul_f16 v63, v137, v49
	v_mfma_f32_32x32x16_f16 a[208:223], v[82:85], v[42:45], a[208:223]
	v_pk_max_f16 v62, v62, v63
	s_nop 0
	v_cndmask_b32_e64 v63, v1, v62, s[48:49]
	v_cndmask_b32_e64 v1, v1, v62, s[50:51]
	v_perm_b32 v77, v1, v63, s20
	v_mfma_f32_32x32x16_f16 a[48:63], v[10:13], v[42:45], a[48:63]
	v_pk_add_f16 v1, v75, v74
	v_pk_add_f16 v42, v76, v77
	s_nop 0
	v_pk_add_f16 v1, v1, v42
	s_nop 0
	v_dot2c_f32_f16_e32 v134, 0x3c003c00, v1
	v_mfma_f32_32x32x16_f16 a[192:207], v[82:85], v[38:41], a[192:207]
	v_pk_mul_f16 v1, v140, v66
	v_pk_mul_f16 v42, v139, v46
	s_nop 0
	v_pk_max_f16 v1, v1, v42
	s_nop 0
	v_cndmask_b32_e64 v42, v138, v1, s[4:5]
	v_mfma_f32_32x32x16_f16 a[64:79], v[10:13], v[38:41], a[64:79]
	v_pk_mul_f16 v38, v140, v67
	v_pk_mul_f16 v39, v139, v47
	v_cndmask_b32_e64 v1, v138, v1, s[6:7]
	v_pk_max_f16 v38, v38, v39
	v_mfma_f32_32x32x16_f16 a[176:191], v[82:85], v[30:33], a[176:191]
	v_pk_mul_f16 v40, v140, v68
	v_pk_mul_f16 v41, v139, v48
	v_cndmask_b32_e64 v39, v138, v38, s[8:9]
	v_cndmask_b32_e64 v38, v138, v38, s[10:11]
	v_mfma_f32_32x32x16_f16 a[112:127], v[10:13], v[30:33], a[112:127]
	v_pk_max_f16 v30, v40, v41
	v_pk_mul_f16 v32, v140, v69
	v_cndmask_b32_e64 v31, v138, v30, s[12:13]
	v_cndmask_b32_e64 v30, v138, v30, s[14:15]
	v_mfma_f32_32x32x16_f16 a[160:175], v[82:85], v[18:21], a[160:175]
	v_pk_mul_f16 v33, v139, v49
	s_nop 0
	v_pk_max_f16 v32, v32, v33
	s_nop 0
	v_cndmask_b32_e64 v33, v138, v32, s[16:17]
	v_cndmask_b32_e64 v32, v138, v32, s[18:19]
	v_mfma_f32_32x32x16_f16 a[128:143], v[10:13], v[18:21], a[128:143]
	v_perm_b32 v18, v1, v42, s20
	v_perm_b32 v19, v38, v39, s20
	v_perm_b32 v20, v30, v31, s20
	v_perm_b32 v21, v32, v33, s20
	v_mfma_f32_32x32x16_f16 a[144:159], v[82:85], v[6:9], a[144:159]
	v_pk_add_f16 v1, v19, v18
	v_pk_add_f16 v30, v20, v21
	s_nop 0
	v_pk_add_f16 v1, v1, v30
	s_nop 0
	v_dot2c_f32_f16_e32 v135, 0x3c003c00, v1
	v_mfma_f32_32x32x16_f16 a[80:95], v[10:13], v[6:9], a[80:95]
	s_waitcnt lgkmcnt(7)
	v_mfma_f32_32x32x16_f16 a[96:111], v[74:77], v[2:5], a[96:111]
	v_mfma_f32_32x32x16_f16 a[0:15], v[18:21], v[2:5], a[0:15]
	s_waitcnt lgkmcnt(6)
	v_mfma_f32_32x32x16_f16 a[240:255], v[74:77], v[14:17], a[240:255]
	v_mfma_f32_32x32x16_f16 a[16:31], v[18:21], v[14:17], a[16:31]
	s_waitcnt lgkmcnt(5)
	v_mfma_f32_32x32x16_f16 a[224:239], v[74:77], v[22:25], a[224:239]
	v_mfma_f32_32x32x16_f16 a[32:47], v[18:21], v[22:25], a[32:47]
	s_waitcnt lgkmcnt(4)
	v_mfma_f32_32x32x16_f16 a[208:223], v[74:77], v[26:29], a[208:223]
	v_mfma_f32_32x32x16_f16 a[48:63], v[18:21], v[26:29], a[48:63]
	s_waitcnt lgkmcnt(3)
	v_mfma_f32_32x32x16_f16 a[192:207], v[74:77], v[34:37], a[192:207]
	v_mfma_f32_32x32x16_f16 a[64:79], v[18:21], v[34:37], a[64:79]
	s_waitcnt lgkmcnt(2)
	v_mfma_f32_32x32x16_f16 a[176:191], v[74:77], v[50:53], a[176:191]
	v_mfma_f32_32x32x16_f16 a[112:127], v[18:21], v[50:53], a[112:127]
	s_waitcnt lgkmcnt(1)
	v_mfma_f32_32x32x16_f16 a[160:175], v[74:77], v[54:57], a[160:175]
	v_mfma_f32_32x32x16_f16 a[128:143], v[18:21], v[54:57], a[128:143]
	s_waitcnt lgkmcnt(0)
	v_mfma_f32_32x32x16_f16 a[144:159], v[74:77], v[58:61], a[144:159]
	v_mfma_f32_32x32x16_f16 a[80:95], v[18:21], v[58:61], a[80:95]
	v_readfirstlane_b32 s1, v0
	s_and_b32 s0, s3, 0xffffff00
	s_andn2_b32 s1, s1, 63
	s_add_i32 s4, s1, s0
	s_lshl_b32 s0, s2, 13
	s_and_b32 s6, s0, 0xe000
	s_ashr_i32 s5, s4, 31
	s_add_u32 s0, s4, s6
	s_addc_u32 s1, s5, 0
	s_lshl_b64 s[2:3], s[0:1], 9
	v_lshrrev_b32_e32 v0, 3, v132
	s_add_u32 s2, s22, s2
	v_and_b32_e32 v3, 12, v0
	s_addc_u32 s3, s23, s3
	v_lshlrev_b32_e32 v0, 9, v3
	v_mov_b32_e32 v1, 0
	v_lshl_add_u64 v[4:5], s[2:3], 0, v[0:1]
	v_lshlrev_b32_e32 v0, 4, v132
	v_and_b32_e32 v0, 0x1f0, v0
	v_lshl_add_u64 v[4:5], v[4:5], 0, v[0:1]
	v_accvgpr_read_b32 v6, a96
	v_accvgpr_read_b32 v7, a240
	v_accvgpr_read_b32 v8, a224
	v_max3_f32 v0, |v6|, |v7|, |v8|
	v_accvgpr_read_b32 v9, a208
	v_accvgpr_read_b32 v14, a192
	v_max3_f32 v0, |v0|, |v9|, |v14|
	v_accvgpr_read_b32 v15, a176
	v_accvgpr_read_b32 v16, a160
	v_max3_f32 v0, |v0|, |v15|, |v16|
	v_accvgpr_read_b32 v10, a144
	v_accvgpr_read_b32 v17, a144
	v_max3_f32 v10, |v0|, |v17|, |v10|
	v_accvgpr_read_b32 v18, a97
	v_accvgpr_read_b32 v19, a241
	v_accvgpr_read_b32 v20, a225
	v_max3_f32 v0, |v18|, |v19|, |v20|
	v_accvgpr_read_b32 v21, a209
	v_accvgpr_read_b32 v22, a193
	v_max3_f32 v0, |v0|, |v21|, |v22|
	v_accvgpr_read_b32 v23, a177
	v_accvgpr_read_b32 v24, a161
	v_max3_f32 v0, |v0|, |v23|, |v24|
	v_accvgpr_read_b32 v11, a145
	v_accvgpr_read_b32 v25, a145
	v_max3_f32 v11, |v0|, |v25|, |v11|
	v_accvgpr_read_b32 v26, a98
	v_accvgpr_read_b32 v27, a242
	v_accvgpr_read_b32 v28, a226
	v_max3_f32 v0, |v26|, |v27|, |v28|
	v_accvgpr_read_b32 v29, a210
	v_accvgpr_read_b32 v30, a194
	v_max3_f32 v0, |v0|, |v29|, |v30|
	v_accvgpr_read_b32 v31, a178
	v_accvgpr_read_b32 v32, a162
	v_max3_f32 v0, |v0|, |v31|, |v32|
	v_accvgpr_read_b32 v12, a146
	v_accvgpr_read_b32 v33, a146
	v_max3_f32 v12, |v0|, |v33|, |v12|
	v_accvgpr_read_b32 v34, a99
	v_accvgpr_read_b32 v35, a243
	v_accvgpr_read_b32 v36, a227
	v_max3_f32 v0, |v34|, |v35|, |v36|
	v_accvgpr_read_b32 v37, a211
	v_accvgpr_read_b32 v38, a195
	v_max3_f32 v0, |v0|, |v37|, |v38|
	v_accvgpr_read_b32 v13, a147
	v_accvgpr_read_b32 v39, a179
	v_accvgpr_read_b32 v40, a163
	v_max3_f32 v0, |v0|, |v39|, |v40|
	v_accvgpr_read_b32 v41, a147
	v_max3_f32 v13, |v0|, |v41|, |v13|
	v_lshlrev_b32_e32 v0, 2, v3
	s_nop 1
	v_max_f32_dpp v10, v10, v10 quad_perm:[1,0,3,2] row_mask:0xf bank_mask:0xf
	v_max_f32_dpp v11, v11, v11 quad_perm:[1,0,3,2] row_mask:0xf bank_mask:0xf
	v_max_f32_dpp v12, v12, v12 quad_perm:[1,0,3,2] row_mask:0xf bank_mask:0xf
	v_max_f32_dpp v13, v13, v13 quad_perm:[1,0,3,2] row_mask:0xf bank_mask:0xf
	v_max_f32_dpp v10, v10, v10 quad_perm:[2,3,0,1] row_mask:0xf bank_mask:0xf
	v_max_f32_dpp v11, v11, v11 quad_perm:[2,3,0,1] row_mask:0xf bank_mask:0xf
	v_max_f32_dpp v12, v12, v12 quad_perm:[2,3,0,1] row_mask:0xf bank_mask:0xf
	v_max_f32_dpp v13, v13, v13 quad_perm:[2,3,0,1] row_mask:0xf bank_mask:0xf
	v_max_f32_dpp v10, v10, v10 row_half_mirror row_mask:0xf bank_mask:0xf
	v_max_f32_dpp v11, v11, v11 row_half_mirror row_mask:0xf bank_mask:0xf
	v_max_f32_dpp v12, v12, v12 row_half_mirror row_mask:0xf bank_mask:0xf
	v_max_f32_dpp v13, v13, v13 row_half_mirror row_mask:0xf bank_mask:0xf
	v_max_f32_dpp v10, v10, v10 row_mirror row_mask:0xf bank_mask:0xf
	v_max_f32_dpp v11, v11, v11 row_mirror row_mask:0xf bank_mask:0xf
	v_max_f32_dpp v12, v12, v12 row_mirror row_mask:0xf bank_mask:0xf
	v_max_f32_dpp v13, v13, v13 row_mirror row_mask:0xf bank_mask:0xf
	s_nop 0
	ds_swizzle_b32 v42, v10 offset:swizzle(SWAP,16)
	s_waitcnt lgkmcnt(0)
	v_max_f32_e32 v10, v10, v42
	ds_swizzle_b32 v3, v12 offset:swizzle(SWAP,16)
	v_rcp_f32_e32 v42, v10
	v_cmp_lt_f32_e32 vcc, 0, v10
	s_waitcnt lgkmcnt(0)
	v_max_f32_e32 v12, v12, v3
	ds_swizzle_b32 v43, v11 offset:swizzle(SWAP,16)
	s_waitcnt lgkmcnt(0)
	v_max_f32_e32 v11, v11, v43
	s_lshl_b32 s2, s6, 2
	v_cndmask_b32_e32 v3, 0, v42, vcc
	v_mul_f32_e32 v6, v3, v6
	v_mul_f32_e32 v7, v3, v7
	v_cvt_pknorm_i16_f32 v6, v6, v7
	v_mul_f32_e32 v7, v3, v8
	v_mul_f32_e32 v8, v3, v9
	v_cvt_pknorm_i16_f32 v7, v7, v8
	v_mul_f32_e32 v8, v3, v14
	v_rcp_f32_e32 v14, v11
	v_mul_f32_e32 v9, v3, v15
	v_cvt_pknorm_i16_f32 v8, v8, v9
	v_mul_f32_e32 v9, v3, v16
	v_mul_f32_e32 v3, v3, v17
	v_cmp_lt_f32_e32 vcc, 0, v11
	v_cvt_pknorm_i16_f32 v9, v9, v3
	global_store_dwordx4 v[4:5], v[6:9], off sc0 sc1
	s_nop 1
	s_add_u32 s6, s24, s2
	v_cndmask_b32_e32 v3, 0, v14, vcc
	v_mul_f32_e32 v6, v3, v18
	v_mul_f32_e32 v7, v3, v19
	v_cvt_pknorm_i16_f32 v6, v6, v7
	v_mul_f32_e32 v7, v3, v20
	v_mul_f32_e32 v8, v3, v21
	v_cvt_pknorm_i16_f32 v7, v7, v8
	v_mul_f32_e32 v8, v3, v22
	v_mul_f32_e32 v9, v3, v23
	v_cvt_pknorm_i16_f32 v8, v8, v9
	v_mul_f32_e32 v9, v3, v24
	v_mul_f32_e32 v3, v3, v25
	v_cvt_pknorm_i16_f32 v9, v9, v3
	v_rcp_f32_e32 v3, v12
	s_addc_u32 s7, s25, 0
	s_lshl_b64 s[2:3], s[4:5], 2
	s_mov_b64 s[4:5], 0x200
	s_add_u32 s2, s6, s2
	v_lshl_add_u64 v[14:15], v[4:5], 0, s[4:5]
	s_mov_b32 s4, 0x38000100
	v_cmp_lt_f32_e32 vcc, 0, v12
	s_addc_u32 s3, s7, s3
	global_store_dwordx4 v[14:15], v[6:9], off sc0 sc1
	s_nop 1
	v_pk_mul_f32 v[6:7], v[10:11], s[4:5] op_sel_hi:[1,0]
	v_cndmask_b32_e32 v3, 0, v3, vcc
	global_store_dwordx2 v0, v[6:7], s[2:3]
	v_mul_f32_e32 v6, v3, v26
	v_mul_f32_e32 v7, v3, v27
	v_cvt_pknorm_i16_f32 v6, v6, v7
	v_mul_f32_e32 v7, v3, v28
	v_mul_f32_e32 v8, v3, v29
	v_cvt_pknorm_i16_f32 v7, v7, v8
	v_mul_f32_e32 v8, v3, v30
	v_mul_f32_e32 v9, v3, v31
	v_cvt_pknorm_i16_f32 v8, v8, v9
	v_mul_f32_e32 v9, v3, v32
	v_mul_f32_e32 v3, v3, v33
	ds_swizzle_b32 v44, v13 offset:swizzle(SWAP,16)
	s_waitcnt lgkmcnt(0)
	v_max_f32_e32 v13, v13, v44
	v_cvt_pknorm_i16_f32 v9, v9, v3
	v_rcp_f32_e32 v3, v13
	v_cmp_lt_f32_e32 vcc, 0, v13
	s_mov_b64 s[6:7], 0x400
	v_lshl_add_u64 v[10:11], v[4:5], 0, s[6:7]
	v_cndmask_b32_e32 v3, 0, v3, vcc
	global_store_dwordx4 v[10:11], v[6:9], off sc0 sc1
	s_nop 1
	v_mul_f32_e32 v6, v3, v34
	v_mul_f32_e32 v7, v3, v35
	v_cvt_pknorm_i16_f32 v6, v6, v7
	v_mul_f32_e32 v7, v3, v36
	v_mul_f32_e32 v8, v3, v37
	v_cvt_pknorm_i16_f32 v7, v7, v8
	v_mul_f32_e32 v8, v3, v38
	v_mul_f32_e32 v9, v3, v39
	v_cvt_pknorm_i16_f32 v8, v8, v9
	v_mul_f32_e32 v9, v3, v40
	v_mul_f32_e32 v3, v3, v41
	s_mov_b64 s[6:7], 0x600
	v_cvt_pknorm_i16_f32 v9, v9, v3
	v_lshl_add_u64 v[10:11], v[4:5], 0, s[6:7]
	global_store_dwordx4 v[10:11], v[6:9], off sc0 sc1
	s_nop 1
	v_pk_mul_f32 v[6:7], v[12:13], s[4:5] op_sel_hi:[1,0]
	v_lshlrev_b32_e32 v2, 2, v132
	global_store_dwordx2 v0, v[6:7], s[2:3] offset:8
	v_accvgpr_read_b32 v42, a100
	v_accvgpr_read_b32 v6, a244
	v_accvgpr_read_b32 v7, a228
	v_max3_f32 v8, |v42|, |v6|, |v7|
	v_accvgpr_read_b32 v9, a212
	v_accvgpr_read_b32 v14, a196
	v_max3_f32 v8, |v8|, |v9|, |v14|
	v_accvgpr_read_b32 v15, a180
	v_accvgpr_read_b32 v16, a164
	v_max3_f32 v8, |v8|, |v15|, |v16|
	v_accvgpr_read_b32 v10, a148
	v_accvgpr_read_b32 v43, a101
	v_accvgpr_read_b32 v17, a148
	v_max3_f32 v8, |v8|, |v17|, |v10|
	v_accvgpr_read_b32 v19, a245
	v_accvgpr_read_b32 v20, a229
	v_max3_f32 v10, |v43|, |v19|, |v20|
	v_accvgpr_read_b32 v21, a213
	v_accvgpr_read_b32 v22, a197
	v_max3_f32 v10, |v10|, |v21|, |v22|
	v_accvgpr_read_b32 v23, a181
	v_accvgpr_read_b32 v24, a165
	v_max3_f32 v10, |v10|, |v23|, |v24|
	v_accvgpr_read_b32 v11, a149
	v_accvgpr_read_b32 v44, a102
	v_accvgpr_read_b32 v25, a149
	v_max3_f32 v11, |v10|, |v25|, |v11|
	v_accvgpr_read_b32 v27, a246
	v_accvgpr_read_b32 v28, a230
	v_max3_f32 v10, |v44|, |v27|, |v28|
	v_accvgpr_read_b32 v29, a214
	v_accvgpr_read_b32 v30, a198
	v_max3_f32 v10, |v10|, |v29|, |v30|
	v_accvgpr_read_b32 v31, a182
	v_accvgpr_read_b32 v32, a166
	v_max3_f32 v10, |v10|, |v31|, |v32|
	v_accvgpr_read_b32 v12, a150
	v_accvgpr_read_b32 v45, a103
	v_accvgpr_read_b32 v33, a150
	v_max3_f32 v12, |v10|, |v33|, |v12|
	v_accvgpr_read_b32 v35, a247
	v_accvgpr_read_b32 v36, a231
	v_max3_f32 v10, |v45|, |v35|, |v36|
	v_accvgpr_read_b32 v37, a215
	v_accvgpr_read_b32 v38, a199
	v_max3_f32 v10, |v10|, |v37|, |v38|
	v_accvgpr_read_b32 v13, a151
	v_accvgpr_read_b32 v39, a183
	v_accvgpr_read_b32 v40, a167
	v_max3_f32 v10, |v10|, |v39|, |v40|
	v_accvgpr_read_b32 v41, a151
	v_max3_f32 v13, |v10|, |v41|, |v13|
	v_mov_b32_e32 v3, v42
	s_nop 1
	v_max_f32_dpp v8, v8, v8 quad_perm:[1,0,3,2] row_mask:0xf bank_mask:0xf
	v_max_f32_dpp v11, v11, v11 quad_perm:[1,0,3,2] row_mask:0xf bank_mask:0xf
	v_max_f32_dpp v12, v12, v12 quad_perm:[1,0,3,2] row_mask:0xf bank_mask:0xf
	v_max_f32_dpp v13, v13, v13 quad_perm:[1,0,3,2] row_mask:0xf bank_mask:0xf
	v_max_f32_dpp v8, v8, v8 quad_perm:[2,3,0,1] row_mask:0xf bank_mask:0xf
	v_max_f32_dpp v11, v11, v11 quad_perm:[2,3,0,1] row_mask:0xf bank_mask:0xf
	v_max_f32_dpp v12, v12, v12 quad_perm:[2,3,0,1] row_mask:0xf bank_mask:0xf
	v_max_f32_dpp v13, v13, v13 quad_perm:[2,3,0,1] row_mask:0xf bank_mask:0xf
	v_max_f32_dpp v8, v8, v8 row_half_mirror row_mask:0xf bank_mask:0xf
	v_max_f32_dpp v11, v11, v11 row_half_mirror row_mask:0xf bank_mask:0xf
	v_max_f32_dpp v12, v12, v12 row_half_mirror row_mask:0xf bank_mask:0xf
	v_max_f32_dpp v13, v13, v13 row_half_mirror row_mask:0xf bank_mask:0xf
	v_max_f32_dpp v8, v8, v8 row_mirror row_mask:0xf bank_mask:0xf
	v_max_f32_dpp v11, v11, v11 row_mirror row_mask:0xf bank_mask:0xf
	v_max_f32_dpp v12, v12, v12 row_mirror row_mask:0xf bank_mask:0xf
	v_max_f32_dpp v13, v13, v13 row_mirror row_mask:0xf bank_mask:0xf
	s_nop 0
	ds_swizzle_b32 v10, v8 offset:swizzle(SWAP,16)
	s_waitcnt lgkmcnt(0)
	v_max_f32_e32 v10, v8, v10
	ds_swizzle_b32 v42, v11 offset:swizzle(SWAP,16)
	v_rcp_f32_e32 v8, v10
	v_cmp_lt_f32_e32 vcc, 0, v10
	s_waitcnt lgkmcnt(0)
	v_max_f32_e32 v11, v11, v42
	v_mov_b32_e32 v18, v43
	s_mov_b64 s[6:7], 0x1000
	v_cndmask_b32_e32 v42, 0, v8, vcc
	v_mul_f32_e32 v3, v42, v3
	v_mul_f32_e32 v6, v42, v6
	v_cvt_pknorm_i16_f32 v6, v3, v6
	v_mul_f32_e32 v3, v42, v7
	v_mul_f32_e32 v7, v42, v9
	v_cvt_pknorm_i16_f32 v7, v3, v7
	v_mul_f32_e32 v3, v42, v14
	v_mul_f32_e32 v8, v42, v15
	v_cvt_pknorm_i16_f32 v8, v3, v8
	v_mul_f32_e32 v3, v42, v16
	v_mul_f32_e32 v9, v42, v17
	v_cvt_pknorm_i16_f32 v9, v3, v9
	v_rcp_f32_e32 v3, v11
	v_cmp_lt_f32_e32 vcc, 0, v11
	v_lshl_add_u64 v[14:15], v[4:5], 0, s[6:7]
	global_store_dwordx4 v[14:15], v[6:9], off sc0 sc1
	s_nop 1
	ds_swizzle_b32 v43, v12 offset:swizzle(SWAP,16)
	v_cndmask_b32_e32 v3, 0, v3, vcc
	v_mul_f32_e32 v6, v3, v18
	v_mul_f32_e32 v7, v3, v19
	v_cvt_pknorm_i16_f32 v6, v6, v7
	v_mul_f32_e32 v7, v3, v20
	v_mul_f32_e32 v8, v3, v21
	v_cvt_pknorm_i16_f32 v7, v7, v8
	v_mul_f32_e32 v8, v3, v22
	v_mul_f32_e32 v9, v3, v23
	v_cvt_pknorm_i16_f32 v8, v8, v9
	v_mul_f32_e32 v9, v3, v24
	v_mul_f32_e32 v3, v3, v25
	s_waitcnt lgkmcnt(0)
	v_max_f32_e32 v12, v12, v43
	v_cvt_pknorm_i16_f32 v9, v9, v3
	v_rcp_f32_e32 v3, v12
	s_mov_b64 s[6:7], 0x1200
	v_cmp_lt_f32_e32 vcc, 0, v12
	v_mov_b32_e32 v26, v44
	v_lshl_add_u64 v[14:15], v[4:5], 0, s[6:7]
	global_store_dwordx4 v[14:15], v[6:9], off sc0 sc1
	s_nop 1
	v_pk_mul_f32 v[6:7], v[10:11], s[4:5] op_sel_hi:[1,0]
	v_cndmask_b32_e32 v3, 0, v3, vcc
	global_store_dwordx2 v0, v[6:7], s[2:3] offset:32
	v_mul_f32_e32 v6, v3, v26
	v_mul_f32_e32 v7, v3, v27
	v_cvt_pknorm_i16_f32 v6, v6, v7
	v_mul_f32_e32 v7, v3, v28
	v_mul_f32_e32 v8, v3, v29
	v_cvt_pknorm_i16_f32 v7, v7, v8
	v_mul_f32_e32 v8, v3, v30
	v_mul_f32_e32 v9, v3, v31
	v_cvt_pknorm_i16_f32 v8, v8, v9
	v_mul_f32_e32 v9, v3, v32
	v_mul_f32_e32 v3, v3, v33
	ds_swizzle_b32 v44, v13 offset:swizzle(SWAP,16)
	s_waitcnt lgkmcnt(0)
	v_max_f32_e32 v13, v13, v44
	v_cvt_pknorm_i16_f32 v9, v9, v3
	v_rcp_f32_e32 v3, v13
	v_cmp_lt_f32_e32 vcc, 0, v13
	v_mov_b32_e32 v34, v45
	s_mov_b64 s[6:7], 0x1400
	v_cndmask_b32_e32 v3, 0, v3, vcc
	v_lshl_add_u64 v[10:11], v[4:5], 0, s[6:7]
	global_store_dwordx4 v[10:11], v[6:9], off sc0 sc1
	s_nop 1
	v_mul_f32_e32 v6, v3, v34
	v_mul_f32_e32 v7, v3, v35
	v_cvt_pknorm_i16_f32 v6, v6, v7
	v_mul_f32_e32 v7, v3, v36
	v_mul_f32_e32 v8, v3, v37
	v_cvt_pknorm_i16_f32 v7, v7, v8
	v_mul_f32_e32 v8, v3, v38
	v_mul_f32_e32 v9, v3, v39
	v_cvt_pknorm_i16_f32 v8, v8, v9
	v_mul_f32_e32 v9, v3, v40
	v_mul_f32_e32 v3, v3, v41
	s_mov_b64 s[6:7], 0x1600
	v_cvt_pknorm_i16_f32 v9, v9, v3
	v_lshl_add_u64 v[10:11], v[4:5], 0, s[6:7]
	global_store_dwordx4 v[10:11], v[6:9], off sc0 sc1
	s_nop 1
	v_pk_mul_f32 v[6:7], v[12:13], s[4:5] op_sel_hi:[1,0]
	v_accvgpr_read_b32 v46, a104
	v_accvgpr_read_b32 v47, a105
	v_accvgpr_read_b32 v48, a106
	v_accvgpr_read_b32 v49, a107
	v_accvgpr_read_b32 v50, a108
	v_accvgpr_read_b32 v51, a109
	v_accvgpr_read_b32 v52, a110
	v_accvgpr_read_b32 v53, a111
	global_store_dwordx2 v0, v[6:7], s[2:3] offset:40
	v_mov_b64_e32 v[42:43], v[46:47]
	v_accvgpr_read_b32 v6, a248
	v_accvgpr_read_b32 v7, a232
	v_max3_f32 v8, |v42|, |v6|, |v7|
	v_accvgpr_read_b32 v9, a216
	v_accvgpr_read_b32 v14, a200
	v_max3_f32 v8, |v8|, |v9|, |v14|
	v_accvgpr_read_b32 v15, a184
	v_accvgpr_read_b32 v16, a168
	v_max3_f32 v8, |v8|, |v15|, |v16|
	v_accvgpr_read_b32 v10, a152
	v_accvgpr_read_b32 v17, a152
	v_max3_f32 v8, |v8|, |v17|, |v10|
	v_accvgpr_read_b32 v19, a249
	v_accvgpr_read_b32 v20, a233
	v_max3_f32 v10, |v43|, |v19|, |v20|
	v_accvgpr_read_b32 v21, a217
	v_accvgpr_read_b32 v22, a201
	v_max3_f32 v10, |v10|, |v21|, |v22|
	v_accvgpr_read_b32 v23, a185
	v_accvgpr_read_b32 v24, a169
	v_max3_f32 v10, |v10|, |v23|, |v24|
	v_accvgpr_read_b32 v11, a153
	v_mov_b64_e32 v[44:45], v[48:49]
	v_accvgpr_read_b32 v25, a153
	v_max3_f32 v11, |v10|, |v25|, |v11|
	v_accvgpr_read_b32 v27, a250
	v_accvgpr_read_b32 v28, a234
	v_max3_f32 v10, |v44|, |v27|, |v28|
	v_accvgpr_read_b32 v29, a218
	v_accvgpr_read_b32 v30, a202
	v_max3_f32 v10, |v10|, |v29|, |v30|
	v_accvgpr_read_b32 v31, a186
	v_accvgpr_read_b32 v32, a170
	v_max3_f32 v10, |v10|, |v31|, |v32|
	v_accvgpr_read_b32 v12, a154
	v_accvgpr_read_b32 v33, a154
	v_max3_f32 v12, |v10|, |v33|, |v12|
	v_accvgpr_read_b32 v35, a251
	v_accvgpr_read_b32 v36, a235
	v_max3_f32 v10, |v45|, |v35|, |v36|
	v_accvgpr_read_b32 v37, a219
	v_accvgpr_read_b32 v38, a203
	v_max3_f32 v10, |v10|, |v37|, |v38|
	v_accvgpr_read_b32 v13, a155
	v_accvgpr_read_b32 v39, a187
	v_accvgpr_read_b32 v40, a171
	v_max3_f32 v10, |v10|, |v39|, |v40|
	v_accvgpr_read_b32 v41, a155
	v_max3_f32 v13, |v10|, |v41|, |v13|
	v_mov_b32_e32 v3, v42
	s_nop 1
	v_max_f32_dpp v8, v8, v8 quad_perm:[1,0,3,2] row_mask:0xf bank_mask:0xf
	v_max_f32_dpp v11, v11, v11 quad_perm:[1,0,3,2] row_mask:0xf bank_mask:0xf
	v_max_f32_dpp v12, v12, v12 quad_perm:[1,0,3,2] row_mask:0xf bank_mask:0xf
	v_max_f32_dpp v13, v13, v13 quad_perm:[1,0,3,2] row_mask:0xf bank_mask:0xf
	v_max_f32_dpp v8, v8, v8 quad_perm:[2,3,0,1] row_mask:0xf bank_mask:0xf
	v_max_f32_dpp v11, v11, v11 quad_perm:[2,3,0,1] row_mask:0xf bank_mask:0xf
	v_max_f32_dpp v12, v12, v12 quad_perm:[2,3,0,1] row_mask:0xf bank_mask:0xf
	v_max_f32_dpp v13, v13, v13 quad_perm:[2,3,0,1] row_mask:0xf bank_mask:0xf
	v_max_f32_dpp v8, v8, v8 row_half_mirror row_mask:0xf bank_mask:0xf
	v_max_f32_dpp v11, v11, v11 row_half_mirror row_mask:0xf bank_mask:0xf
	v_max_f32_dpp v12, v12, v12 row_half_mirror row_mask:0xf bank_mask:0xf
	v_max_f32_dpp v13, v13, v13 row_half_mirror row_mask:0xf bank_mask:0xf
	v_max_f32_dpp v8, v8, v8 row_mirror row_mask:0xf bank_mask:0xf
	v_max_f32_dpp v11, v11, v11 row_mirror row_mask:0xf bank_mask:0xf
	v_max_f32_dpp v12, v12, v12 row_mirror row_mask:0xf bank_mask:0xf
	v_max_f32_dpp v13, v13, v13 row_mirror row_mask:0xf bank_mask:0xf
	s_nop 0
	ds_swizzle_b32 v10, v8 offset:swizzle(SWAP,16)
	s_waitcnt lgkmcnt(0)
	v_max_f32_e32 v10, v8, v10
	ds_swizzle_b32 v42, v11 offset:swizzle(SWAP,16)
	v_rcp_f32_e32 v8, v10
	v_cmp_lt_f32_e32 vcc, 0, v10
	s_waitcnt lgkmcnt(0)
	v_max_f32_e32 v11, v11, v42
	v_mov_b32_e32 v18, v43
	s_mov_b64 s[6:7], 0x2000
	v_cndmask_b32_e32 v42, 0, v8, vcc
	v_mul_f32_e32 v3, v42, v3
	v_mul_f32_e32 v6, v42, v6
	v_cvt_pknorm_i16_f32 v6, v3, v6
	v_mul_f32_e32 v3, v42, v7
	v_mul_f32_e32 v7, v42, v9
	v_cvt_pknorm_i16_f32 v7, v3, v7
	v_mul_f32_e32 v3, v42, v14
	v_mul_f32_e32 v8, v42, v15
	v_cvt_pknorm_i16_f32 v8, v3, v8
	v_mul_f32_e32 v3, v42, v16
	v_mul_f32_e32 v9, v42, v17
	v_cvt_pknorm_i16_f32 v9, v3, v9
	v_rcp_f32_e32 v3, v11
	v_cmp_lt_f32_e32 vcc, 0, v11
	v_lshl_add_u64 v[14:15], v[4:5], 0, s[6:7]
	global_store_dwordx4 v[14:15], v[6:9], off sc0 sc1
	s_nop 1
	ds_swizzle_b32 v43, v12 offset:swizzle(SWAP,16)
	v_cndmask_b32_e32 v3, 0, v3, vcc
	v_mul_f32_e32 v6, v3, v18
	v_mul_f32_e32 v7, v3, v19
	v_cvt_pknorm_i16_f32 v6, v6, v7
	v_mul_f32_e32 v7, v3, v20
	v_mul_f32_e32 v8, v3, v21
	v_cvt_pknorm_i16_f32 v7, v7, v8
	v_mul_f32_e32 v8, v3, v22
	v_mul_f32_e32 v9, v3, v23
	v_cvt_pknorm_i16_f32 v8, v8, v9
	v_mul_f32_e32 v9, v3, v24
	v_mul_f32_e32 v3, v3, v25
	s_waitcnt lgkmcnt(0)
	v_max_f32_e32 v12, v12, v43
	v_cvt_pknorm_i16_f32 v9, v9, v3
	v_rcp_f32_e32 v3, v12
	s_mov_b64 s[6:7], 0x2200
	v_cmp_lt_f32_e32 vcc, 0, v12
	v_mov_b32_e32 v26, v44
	v_lshl_add_u64 v[14:15], v[4:5], 0, s[6:7]
	global_store_dwordx4 v[14:15], v[6:9], off sc0 sc1
	s_nop 1
	v_pk_mul_f32 v[6:7], v[10:11], s[4:5] op_sel_hi:[1,0]
	v_cndmask_b32_e32 v3, 0, v3, vcc
	global_store_dwordx2 v0, v[6:7], s[2:3] offset:64
	v_mul_f32_e32 v6, v3, v26
	v_mul_f32_e32 v7, v3, v27
	v_cvt_pknorm_i16_f32 v6, v6, v7
	v_mul_f32_e32 v7, v3, v28
	v_mul_f32_e32 v8, v3, v29
	v_cvt_pknorm_i16_f32 v7, v7, v8
	v_mul_f32_e32 v8, v3, v30
	v_mul_f32_e32 v9, v3, v31
	v_cvt_pknorm_i16_f32 v8, v8, v9
	v_mul_f32_e32 v9, v3, v32
	v_mul_f32_e32 v3, v3, v33
	ds_swizzle_b32 v44, v13 offset:swizzle(SWAP,16)
	s_waitcnt lgkmcnt(0)
	v_max_f32_e32 v13, v13, v44
	v_cvt_pknorm_i16_f32 v9, v9, v3
	v_rcp_f32_e32 v3, v13
	v_cmp_lt_f32_e32 vcc, 0, v13
	v_mov_b32_e32 v34, v45
	s_mov_b64 s[6:7], 0x2400
	v_cndmask_b32_e32 v3, 0, v3, vcc
	v_lshl_add_u64 v[10:11], v[4:5], 0, s[6:7]
	global_store_dwordx4 v[10:11], v[6:9], off sc0 sc1
	s_nop 1
	v_mul_f32_e32 v6, v3, v34
	v_mul_f32_e32 v7, v3, v35
	v_cvt_pknorm_i16_f32 v6, v6, v7
	v_mul_f32_e32 v7, v3, v36
	v_mul_f32_e32 v8, v3, v37
	v_cvt_pknorm_i16_f32 v7, v7, v8
	v_mul_f32_e32 v8, v3, v38
	v_mul_f32_e32 v9, v3, v39
	v_cvt_pknorm_i16_f32 v8, v8, v9
	v_mul_f32_e32 v9, v3, v40
	v_mul_f32_e32 v3, v3, v41
	s_mov_b64 s[6:7], 0x2600
	v_cvt_pknorm_i16_f32 v9, v9, v3
	v_lshl_add_u64 v[10:11], v[4:5], 0, s[6:7]
	global_store_dwordx4 v[10:11], v[6:9], off sc0 sc1
	s_nop 1
	v_pk_mul_f32 v[6:7], v[12:13], s[4:5] op_sel_hi:[1,0]
	v_mov_b64_e32 v[46:47], v[50:51]
	v_mov_b64_e32 v[48:49], v[52:53]
	global_store_dwordx2 v0, v[6:7], s[2:3] offset:72
	v_mov_b64_e32 v[32:33], v[46:47]
	v_accvgpr_read_b32 v6, a252
	v_accvgpr_read_b32 v7, a236
	v_max3_f32 v8, |v32|, |v6|, |v7|
	v_accvgpr_read_b32 v9, a220
	v_accvgpr_read_b32 v14, a204
	v_max3_f32 v8, |v8|, |v9|, |v14|
	v_accvgpr_read_b32 v15, a188
	v_accvgpr_read_b32 v16, a172
	v_max3_f32 v8, |v8|, |v15|, |v16|
	v_accvgpr_read_b32 v10, a156
	v_accvgpr_read_b32 v17, a156
	v_max3_f32 v8, |v8|, |v17|, |v10|
	v_accvgpr_read_b32 v19, a253
	v_accvgpr_read_b32 v20, a237
	v_max3_f32 v10, |v33|, |v19|, |v20|
	v_accvgpr_read_b32 v21, a221
	v_accvgpr_read_b32 v22, a205
	v_max3_f32 v10, |v10|, |v21|, |v22|
	v_accvgpr_read_b32 v23, a189
	v_accvgpr_read_b32 v24, a173
	v_max3_f32 v10, |v10|, |v23|, |v24|
	v_accvgpr_read_b32 v11, a157
	v_mov_b64_e32 v[34:35], v[48:49]
	v_accvgpr_read_b32 v25, a157
	v_max3_f32 v11, |v10|, |v25|, |v11|
	v_accvgpr_read_b32 v27, a254
	v_accvgpr_read_b32 v28, a238
	v_max3_f32 v10, |v34|, |v27|, |v28|
	v_accvgpr_read_b32 v29, a222
	v_accvgpr_read_b32 v30, a206
	v_max3_f32 v10, |v10|, |v29|, |v30|
	v_mov_b32_e32 v3, v32
	v_accvgpr_read_b32 v31, a190
	v_accvgpr_read_b32 v32, a174
	v_max3_f32 v10, |v10|, |v31|, |v32|
	v_accvgpr_read_b32 v12, a158
	v_mov_b32_e32 v18, v33
	v_mov_b32_e32 v26, v34
	v_accvgpr_read_b32 v33, a158
	v_max3_f32 v12, |v10|, |v33|, |v12|
	v_mov_b32_e32 v34, v35
	v_accvgpr_read_b32 v35, a255
	v_accvgpr_read_b32 v36, a239
	v_max3_f32 v10, |v34|, |v35|, |v36|
	v_accvgpr_read_b32 v37, a223
	v_accvgpr_read_b32 v38, a207
	v_max3_f32 v10, |v10|, |v37|, |v38|
	v_accvgpr_read_b32 v13, a159
	v_accvgpr_read_b32 v39, a191
	v_accvgpr_read_b32 v40, a175
	v_max3_f32 v10, |v10|, |v39|, |v40|
	v_accvgpr_read_b32 v41, a159
	v_max3_f32 v13, |v10|, |v41|, |v13|
	s_mov_b64 s[6:7], 0x3000
	s_nop 1
	v_max_f32_dpp v8, v8, v8 quad_perm:[1,0,3,2] row_mask:0xf bank_mask:0xf
	v_max_f32_dpp v11, v11, v11 quad_perm:[1,0,3,2] row_mask:0xf bank_mask:0xf
	v_max_f32_dpp v12, v12, v12 quad_perm:[1,0,3,2] row_mask:0xf bank_mask:0xf
	v_max_f32_dpp v13, v13, v13 quad_perm:[1,0,3,2] row_mask:0xf bank_mask:0xf
	v_max_f32_dpp v8, v8, v8 quad_perm:[2,3,0,1] row_mask:0xf bank_mask:0xf
	v_max_f32_dpp v11, v11, v11 quad_perm:[2,3,0,1] row_mask:0xf bank_mask:0xf
	v_max_f32_dpp v12, v12, v12 quad_perm:[2,3,0,1] row_mask:0xf bank_mask:0xf
	v_max_f32_dpp v13, v13, v13 quad_perm:[2,3,0,1] row_mask:0xf bank_mask:0xf
	v_max_f32_dpp v8, v8, v8 row_half_mirror row_mask:0xf bank_mask:0xf
	v_max_f32_dpp v11, v11, v11 row_half_mirror row_mask:0xf bank_mask:0xf
	v_max_f32_dpp v12, v12, v12 row_half_mirror row_mask:0xf bank_mask:0xf
	v_max_f32_dpp v13, v13, v13 row_half_mirror row_mask:0xf bank_mask:0xf
	v_max_f32_dpp v8, v8, v8 row_mirror row_mask:0xf bank_mask:0xf
	v_max_f32_dpp v11, v11, v11 row_mirror row_mask:0xf bank_mask:0xf
	v_max_f32_dpp v12, v12, v12 row_mirror row_mask:0xf bank_mask:0xf
	v_max_f32_dpp v13, v13, v13 row_mirror row_mask:0xf bank_mask:0xf
	s_nop 0
	ds_swizzle_b32 v10, v8 offset:swizzle(SWAP,16)
	s_waitcnt lgkmcnt(0)
	v_max_f32_e32 v10, v8, v10
	ds_swizzle_b32 v42, v11 offset:swizzle(SWAP,16)
	v_rcp_f32_e32 v8, v10
	v_cmp_lt_f32_e32 vcc, 0, v10
	s_waitcnt lgkmcnt(0)
	v_max_f32_e32 v11, v11, v42
	ds_swizzle_b32 v43, v12 offset:swizzle(SWAP,16)
	s_waitcnt lgkmcnt(0)
	v_max_f32_e32 v12, v12, v43
	ds_swizzle_b32 v44, v13 offset:swizzle(SWAP,16)
	v_cndmask_b32_e32 v42, 0, v8, vcc
	v_mul_f32_e32 v3, v42, v3
	v_mul_f32_e32 v6, v42, v6
	v_cvt_pknorm_i16_f32 v6, v3, v6
	v_mul_f32_e32 v3, v42, v7
	v_mul_f32_e32 v7, v42, v9
	v_cvt_pknorm_i16_f32 v7, v3, v7
	v_mul_f32_e32 v3, v42, v14
	v_mul_f32_e32 v8, v42, v15
	v_cvt_pknorm_i16_f32 v8, v3, v8
	v_mul_f32_e32 v3, v42, v16
	v_mul_f32_e32 v9, v42, v17
	v_cvt_pknorm_i16_f32 v9, v3, v9
	v_rcp_f32_e32 v3, v11
	v_cmp_lt_f32_e32 vcc, 0, v11
	v_lshl_add_u64 v[14:15], v[4:5], 0, s[6:7]
	global_store_dwordx4 v[14:15], v[6:9], off sc0 sc1
	s_nop 1
	s_mov_b64 s[6:7], 0x3200
	v_cndmask_b32_e32 v3, 0, v3, vcc
	v_mul_f32_e32 v6, v3, v18
	v_mul_f32_e32 v7, v3, v19
	v_cvt_pknorm_i16_f32 v6, v6, v7
	v_mul_f32_e32 v7, v3, v20
	v_mul_f32_e32 v8, v3, v21
	v_cvt_pknorm_i16_f32 v7, v7, v8
	v_mul_f32_e32 v8, v3, v22
	v_mul_f32_e32 v9, v3, v23
	v_cvt_pknorm_i16_f32 v8, v8, v9
	v_mul_f32_e32 v9, v3, v24
	v_mul_f32_e32 v3, v3, v25
	v_cvt_pknorm_i16_f32 v9, v9, v3
	v_rcp_f32_e32 v3, v12
	v_cmp_lt_f32_e32 vcc, 0, v12
	v_lshl_add_u64 v[14:15], v[4:5], 0, s[6:7]
	global_store_dwordx4 v[14:15], v[6:9], off sc0 sc1
	s_nop 1
	v_pk_mul_f32 v[6:7], v[10:11], s[4:5] op_sel_hi:[1,0]
	v_cndmask_b32_e32 v3, 0, v3, vcc
	global_store_dwordx2 v0, v[6:7], s[2:3] offset:96
	v_mul_f32_e32 v6, v3, v26
	v_mul_f32_e32 v7, v3, v27
	v_cvt_pknorm_i16_f32 v6, v6, v7
	v_mul_f32_e32 v7, v3, v28
	v_mul_f32_e32 v8, v3, v29
	v_cvt_pknorm_i16_f32 v7, v7, v8
	v_mul_f32_e32 v8, v3, v30
	v_mul_f32_e32 v9, v3, v31
	v_cvt_pknorm_i16_f32 v8, v8, v9
	v_mul_f32_e32 v9, v3, v32
	v_mul_f32_e32 v3, v3, v33
	s_waitcnt lgkmcnt(0)
	v_max_f32_e32 v13, v13, v44
	v_cvt_pknorm_i16_f32 v9, v9, v3
	v_rcp_f32_e32 v3, v13
	v_cmp_lt_f32_e32 vcc, 0, v13
	s_mov_b64 s[6:7], 0x3400
	v_lshl_add_u64 v[10:11], v[4:5], 0, s[6:7]
	v_cndmask_b32_e32 v3, 0, v3, vcc
	global_store_dwordx4 v[10:11], v[6:9], off sc0 sc1
	s_nop 1
	v_mul_f32_e32 v6, v3, v34
	v_mul_f32_e32 v7, v3, v35
	v_cvt_pknorm_i16_f32 v6, v6, v7
	v_mul_f32_e32 v7, v3, v36
	v_mul_f32_e32 v8, v3, v37
	v_cvt_pknorm_i16_f32 v7, v7, v8
	v_mul_f32_e32 v8, v3, v38
	v_mul_f32_e32 v9, v3, v39
	v_cvt_pknorm_i16_f32 v8, v8, v9
	v_mul_f32_e32 v9, v3, v40
	v_mul_f32_e32 v3, v3, v41
	s_mov_b64 s[6:7], 0x3600
	v_cvt_pknorm_i16_f32 v9, v9, v3
	v_lshl_add_u64 v[10:11], v[4:5], 0, s[6:7]
	global_store_dwordx4 v[10:11], v[6:9], off sc0 sc1
	s_nop 1
	v_pk_mul_f32 v[6:7], v[12:13], s[4:5] op_sel_hi:[1,0]
	global_store_dwordx2 v0, v[6:7], s[2:3] offset:104
	v_accvgpr_read_b32 v3, a0
	v_accvgpr_read_b32 v6, a16
	v_accvgpr_read_b32 v7, a32
	v_max3_f32 v8, |v3|, |v6|, |v7|
	v_accvgpr_read_b32 v9, a48
	v_accvgpr_read_b32 v14, a64
	v_max3_f32 v8, |v8|, |v9|, |v14|
	v_accvgpr_read_b32 v15, a112
	v_accvgpr_read_b32 v16, a128
	v_max3_f32 v8, |v8|, |v15|, |v16|
	v_accvgpr_read_b32 v10, a80
	v_accvgpr_read_b32 v17, a80
	v_max3_f32 v8, |v8|, |v17|, |v10|
	v_accvgpr_read_b32 v18, a1
	v_accvgpr_read_b32 v19, a17
	v_accvgpr_read_b32 v20, a33
	v_max3_f32 v10, |v18|, |v19|, |v20|
	v_accvgpr_read_b32 v21, a49
	v_accvgpr_read_b32 v22, a65
	v_max3_f32 v10, |v10|, |v21|, |v22|
	v_accvgpr_read_b32 v23, a113
	v_accvgpr_read_b32 v24, a129
	v_max3_f32 v10, |v10|, |v23|, |v24|
	v_accvgpr_read_b32 v11, a81
	v_accvgpr_read_b32 v25, a81
	v_max3_f32 v11, |v10|, |v25|, |v11|
	v_accvgpr_read_b32 v26, a2
	v_accvgpr_read_b32 v27, a18
	v_accvgpr_read_b32 v28, a34
	v_max3_f32 v10, |v26|, |v27|, |v28|
	v_accvgpr_read_b32 v29, a50
	v_accvgpr_read_b32 v30, a66
	v_max3_f32 v10, |v10|, |v29|, |v30|
	v_accvgpr_read_b32 v31, a114
	v_accvgpr_read_b32 v32, a130
	v_max3_f32 v10, |v10|, |v31|, |v32|
	v_accvgpr_read_b32 v12, a82
	v_accvgpr_read_b32 v33, a82
	v_max3_f32 v12, |v10|, |v33|, |v12|
	v_accvgpr_read_b32 v34, a3
	v_accvgpr_read_b32 v35, a19
	v_accvgpr_read_b32 v36, a35
	v_max3_f32 v10, |v34|, |v35|, |v36|
	v_accvgpr_read_b32 v37, a51
	v_accvgpr_read_b32 v38, a67
	v_max3_f32 v10, |v10|, |v37|, |v38|
	v_accvgpr_read_b32 v13, a83
	v_accvgpr_read_b32 v39, a115
	v_accvgpr_read_b32 v40, a131
	v_max3_f32 v10, |v10|, |v39|, |v40|
	v_accvgpr_read_b32 v41, a83
	v_max3_f32 v13, |v10|, |v41|, |v13|
	s_mov_b64 s[6:7], 0x4000
	s_nop 1
	v_max_f32_dpp v8, v8, v8 quad_perm:[1,0,3,2] row_mask:0xf bank_mask:0xf
	v_max_f32_dpp v11, v11, v11 quad_perm:[1,0,3,2] row_mask:0xf bank_mask:0xf
	v_max_f32_dpp v12, v12, v12 quad_perm:[1,0,3,2] row_mask:0xf bank_mask:0xf
	v_max_f32_dpp v13, v13, v13 quad_perm:[1,0,3,2] row_mask:0xf bank_mask:0xf
	v_max_f32_dpp v8, v8, v8 quad_perm:[2,3,0,1] row_mask:0xf bank_mask:0xf
	v_max_f32_dpp v11, v11, v11 quad_perm:[2,3,0,1] row_mask:0xf bank_mask:0xf
	v_max_f32_dpp v12, v12, v12 quad_perm:[2,3,0,1] row_mask:0xf bank_mask:0xf
	v_max_f32_dpp v13, v13, v13 quad_perm:[2,3,0,1] row_mask:0xf bank_mask:0xf
	v_max_f32_dpp v8, v8, v8 row_half_mirror row_mask:0xf bank_mask:0xf
	v_max_f32_dpp v11, v11, v11 row_half_mirror row_mask:0xf bank_mask:0xf
	v_max_f32_dpp v12, v12, v12 row_half_mirror row_mask:0xf bank_mask:0xf
	v_max_f32_dpp v13, v13, v13 row_half_mirror row_mask:0xf bank_mask:0xf
	v_max_f32_dpp v8, v8, v8 row_mirror row_mask:0xf bank_mask:0xf
	v_max_f32_dpp v11, v11, v11 row_mirror row_mask:0xf bank_mask:0xf
	v_max_f32_dpp v12, v12, v12 row_mirror row_mask:0xf bank_mask:0xf
	v_max_f32_dpp v13, v13, v13 row_mirror row_mask:0xf bank_mask:0xf
	s_nop 0
	ds_swizzle_b32 v10, v8 offset:swizzle(SWAP,16)
	s_waitcnt lgkmcnt(0)
	v_max_f32_e32 v10, v8, v10
	ds_swizzle_b32 v42, v11 offset:swizzle(SWAP,16)
	v_rcp_f32_e32 v8, v10
	v_cmp_lt_f32_e32 vcc, 0, v10
	s_waitcnt lgkmcnt(0)
	v_max_f32_e32 v11, v11, v42
	ds_swizzle_b32 v43, v12 offset:swizzle(SWAP,16)
	s_waitcnt lgkmcnt(0)
	v_max_f32_e32 v12, v12, v43
	ds_swizzle_b32 v44, v13 offset:swizzle(SWAP,16)
	v_cndmask_b32_e32 v42, 0, v8, vcc
	v_mul_f32_e32 v3, v42, v3
	v_mul_f32_e32 v6, v42, v6
	v_cvt_pknorm_i16_f32 v6, v3, v6
	v_mul_f32_e32 v3, v42, v7
	v_mul_f32_e32 v7, v42, v9
	v_cvt_pknorm_i16_f32 v7, v3, v7
	v_mul_f32_e32 v3, v42, v14
	v_mul_f32_e32 v8, v42, v15
	v_cvt_pknorm_i16_f32 v8, v3, v8
	v_mul_f32_e32 v3, v42, v16
	v_mul_f32_e32 v9, v42, v17
	v_cvt_pknorm_i16_f32 v9, v3, v9
	v_rcp_f32_e32 v3, v11
	v_cmp_lt_f32_e32 vcc, 0, v11
	v_lshl_add_u64 v[14:15], v[4:5], 0, s[6:7]
	global_store_dwordx4 v[14:15], v[6:9], off sc0 sc1
	s_nop 1
	s_mov_b64 s[6:7], 0x4200
	v_cndmask_b32_e32 v3, 0, v3, vcc
	v_mul_f32_e32 v6, v3, v18
	v_mul_f32_e32 v7, v3, v19
	v_cvt_pknorm_i16_f32 v6, v6, v7
	v_mul_f32_e32 v7, v3, v20
	v_mul_f32_e32 v8, v3, v21
	v_cvt_pknorm_i16_f32 v7, v7, v8
	v_mul_f32_e32 v8, v3, v22
	v_mul_f32_e32 v9, v3, v23
	v_cvt_pknorm_i16_f32 v8, v8, v9
	v_mul_f32_e32 v9, v3, v24
	v_mul_f32_e32 v3, v3, v25
	v_cvt_pknorm_i16_f32 v9, v9, v3
	v_rcp_f32_e32 v3, v12
	v_cmp_lt_f32_e32 vcc, 0, v12
	v_lshl_add_u64 v[14:15], v[4:5], 0, s[6:7]
	global_store_dwordx4 v[14:15], v[6:9], off sc0 sc1
	s_nop 1
	v_pk_mul_f32 v[6:7], v[10:11], s[4:5] op_sel_hi:[1,0]
	v_cndmask_b32_e32 v3, 0, v3, vcc
	global_store_dwordx2 v0, v[6:7], s[2:3] offset:128
	v_mul_f32_e32 v6, v3, v26
	v_mul_f32_e32 v7, v3, v27
	v_cvt_pknorm_i16_f32 v6, v6, v7
	v_mul_f32_e32 v7, v3, v28
	v_mul_f32_e32 v8, v3, v29
	v_cvt_pknorm_i16_f32 v7, v7, v8
	v_mul_f32_e32 v8, v3, v30
	v_mul_f32_e32 v9, v3, v31
	v_cvt_pknorm_i16_f32 v8, v8, v9
	v_mul_f32_e32 v9, v3, v32
	v_mul_f32_e32 v3, v3, v33
	s_waitcnt lgkmcnt(0)
	v_max_f32_e32 v13, v13, v44
	v_cvt_pknorm_i16_f32 v9, v9, v3
	v_rcp_f32_e32 v3, v13
	v_cmp_lt_f32_e32 vcc, 0, v13
	s_mov_b64 s[6:7], 0x4400
	v_lshl_add_u64 v[10:11], v[4:5], 0, s[6:7]
	v_cndmask_b32_e32 v3, 0, v3, vcc
	global_store_dwordx4 v[10:11], v[6:9], off sc0 sc1
	s_nop 1
	v_mul_f32_e32 v6, v3, v34
	v_mul_f32_e32 v7, v3, v35
	v_cvt_pknorm_i16_f32 v6, v6, v7
	v_mul_f32_e32 v7, v3, v36
	v_mul_f32_e32 v8, v3, v37
	v_cvt_pknorm_i16_f32 v7, v7, v8
	v_mul_f32_e32 v8, v3, v38
	v_mul_f32_e32 v9, v3, v39
	v_cvt_pknorm_i16_f32 v8, v8, v9
	v_mul_f32_e32 v9, v3, v40
	v_mul_f32_e32 v3, v3, v41
	s_mov_b64 s[6:7], 0x4600
	v_cvt_pknorm_i16_f32 v9, v9, v3
	v_lshl_add_u64 v[10:11], v[4:5], 0, s[6:7]
	global_store_dwordx4 v[10:11], v[6:9], off sc0 sc1
	s_nop 1
	v_pk_mul_f32 v[6:7], v[12:13], s[4:5] op_sel_hi:[1,0]
	global_store_dwordx2 v0, v[6:7], s[2:3] offset:136
	v_accvgpr_read_b32 v3, a4
	v_accvgpr_read_b32 v6, a20
	v_accvgpr_read_b32 v7, a36
	v_max3_f32 v8, |v3|, |v6|, |v7|
	v_accvgpr_read_b32 v9, a52
	v_accvgpr_read_b32 v14, a68
	v_max3_f32 v8, |v8|, |v9|, |v14|
	v_accvgpr_read_b32 v15, a116
	v_accvgpr_read_b32 v16, a132
	v_max3_f32 v8, |v8|, |v15|, |v16|
	v_accvgpr_read_b32 v10, a84
	v_accvgpr_read_b32 v17, a84
	v_max3_f32 v8, |v8|, |v17|, |v10|
	v_accvgpr_read_b32 v18, a5
	v_accvgpr_read_b32 v19, a21
	v_accvgpr_read_b32 v20, a37
	v_max3_f32 v10, |v18|, |v19|, |v20|
	v_accvgpr_read_b32 v21, a53
	v_accvgpr_read_b32 v22, a69
	v_max3_f32 v10, |v10|, |v21|, |v22|
	v_accvgpr_read_b32 v23, a117
	v_accvgpr_read_b32 v24, a133
	v_max3_f32 v10, |v10|, |v23|, |v24|
	v_accvgpr_read_b32 v11, a85
	v_accvgpr_read_b32 v25, a85
	v_max3_f32 v11, |v10|, |v25|, |v11|
	v_accvgpr_read_b32 v26, a6
	v_accvgpr_read_b32 v27, a22
	v_accvgpr_read_b32 v28, a38
	v_max3_f32 v10, |v26|, |v27|, |v28|
	v_accvgpr_read_b32 v29, a54
	v_accvgpr_read_b32 v30, a70
	v_max3_f32 v10, |v10|, |v29|, |v30|
	v_accvgpr_read_b32 v31, a118
	v_accvgpr_read_b32 v32, a134
	v_max3_f32 v10, |v10|, |v31|, |v32|
	v_accvgpr_read_b32 v12, a86
	v_accvgpr_read_b32 v33, a86
	v_max3_f32 v12, |v10|, |v33|, |v12|
	v_accvgpr_read_b32 v34, a7
	v_accvgpr_read_b32 v35, a23
	v_accvgpr_read_b32 v36, a39
	v_max3_f32 v10, |v34|, |v35|, |v36|
	v_accvgpr_read_b32 v37, a55
	v_accvgpr_read_b32 v38, a71
	v_max3_f32 v10, |v10|, |v37|, |v38|
	v_accvgpr_read_b32 v13, a87
	v_accvgpr_read_b32 v39, a119
	v_accvgpr_read_b32 v40, a135
	v_max3_f32 v10, |v10|, |v39|, |v40|
	v_accvgpr_read_b32 v41, a87
	v_max3_f32 v13, |v10|, |v41|, |v13|
	s_mov_b64 s[6:7], 0x5000
	s_nop 1
	v_max_f32_dpp v8, v8, v8 quad_perm:[1,0,3,2] row_mask:0xf bank_mask:0xf
	v_max_f32_dpp v11, v11, v11 quad_perm:[1,0,3,2] row_mask:0xf bank_mask:0xf
	v_max_f32_dpp v12, v12, v12 quad_perm:[1,0,3,2] row_mask:0xf bank_mask:0xf
	v_max_f32_dpp v13, v13, v13 quad_perm:[1,0,3,2] row_mask:0xf bank_mask:0xf
	v_max_f32_dpp v8, v8, v8 quad_perm:[2,3,0,1] row_mask:0xf bank_mask:0xf
	v_max_f32_dpp v11, v11, v11 quad_perm:[2,3,0,1] row_mask:0xf bank_mask:0xf
	v_max_f32_dpp v12, v12, v12 quad_perm:[2,3,0,1] row_mask:0xf bank_mask:0xf
	v_max_f32_dpp v13, v13, v13 quad_perm:[2,3,0,1] row_mask:0xf bank_mask:0xf
	v_max_f32_dpp v8, v8, v8 row_half_mirror row_mask:0xf bank_mask:0xf
	v_max_f32_dpp v11, v11, v11 row_half_mirror row_mask:0xf bank_mask:0xf
	v_max_f32_dpp v12, v12, v12 row_half_mirror row_mask:0xf bank_mask:0xf
	v_max_f32_dpp v13, v13, v13 row_half_mirror row_mask:0xf bank_mask:0xf
	v_max_f32_dpp v8, v8, v8 row_mirror row_mask:0xf bank_mask:0xf
	v_max_f32_dpp v11, v11, v11 row_mirror row_mask:0xf bank_mask:0xf
	v_max_f32_dpp v12, v12, v12 row_mirror row_mask:0xf bank_mask:0xf
	v_max_f32_dpp v13, v13, v13 row_mirror row_mask:0xf bank_mask:0xf
	s_nop 0
	ds_swizzle_b32 v10, v8 offset:swizzle(SWAP,16)
	s_waitcnt lgkmcnt(0)
	v_max_f32_e32 v10, v8, v10
	ds_swizzle_b32 v42, v11 offset:swizzle(SWAP,16)
	v_rcp_f32_e32 v8, v10
	v_cmp_lt_f32_e32 vcc, 0, v10
	s_waitcnt lgkmcnt(0)
	v_max_f32_e32 v11, v11, v42
	ds_swizzle_b32 v43, v12 offset:swizzle(SWAP,16)
	s_waitcnt lgkmcnt(0)
	v_max_f32_e32 v12, v12, v43
	ds_swizzle_b32 v44, v13 offset:swizzle(SWAP,16)
	v_cndmask_b32_e32 v42, 0, v8, vcc
	v_mul_f32_e32 v3, v42, v3
	v_mul_f32_e32 v6, v42, v6
	v_cvt_pknorm_i16_f32 v6, v3, v6
	v_mul_f32_e32 v3, v42, v7
	v_mul_f32_e32 v7, v42, v9
	v_cvt_pknorm_i16_f32 v7, v3, v7
	v_mul_f32_e32 v3, v42, v14
	v_mul_f32_e32 v8, v42, v15
	v_cvt_pknorm_i16_f32 v8, v3, v8
	v_mul_f32_e32 v3, v42, v16
	v_mul_f32_e32 v9, v42, v17
	v_cvt_pknorm_i16_f32 v9, v3, v9
	v_rcp_f32_e32 v3, v11
	v_cmp_lt_f32_e32 vcc, 0, v11
	v_lshl_add_u64 v[14:15], v[4:5], 0, s[6:7]
	global_store_dwordx4 v[14:15], v[6:9], off sc0 sc1
	s_nop 1
	s_mov_b64 s[6:7], 0x5200
	v_cndmask_b32_e32 v3, 0, v3, vcc
	v_mul_f32_e32 v6, v3, v18
	v_mul_f32_e32 v7, v3, v19
	v_cvt_pknorm_i16_f32 v6, v6, v7
	v_mul_f32_e32 v7, v3, v20
	v_mul_f32_e32 v8, v3, v21
	v_cvt_pknorm_i16_f32 v7, v7, v8
	v_mul_f32_e32 v8, v3, v22
	v_mul_f32_e32 v9, v3, v23
	v_cvt_pknorm_i16_f32 v8, v8, v9
	v_mul_f32_e32 v9, v3, v24
	v_mul_f32_e32 v3, v3, v25
	v_cvt_pknorm_i16_f32 v9, v9, v3
	v_rcp_f32_e32 v3, v12
	v_cmp_lt_f32_e32 vcc, 0, v12
	v_lshl_add_u64 v[14:15], v[4:5], 0, s[6:7]
	global_store_dwordx4 v[14:15], v[6:9], off sc0 sc1
	s_nop 1
	v_pk_mul_f32 v[6:7], v[10:11], s[4:5] op_sel_hi:[1,0]
	v_cndmask_b32_e32 v3, 0, v3, vcc
	global_store_dwordx2 v0, v[6:7], s[2:3] offset:160
	v_mul_f32_e32 v6, v3, v26
	v_mul_f32_e32 v7, v3, v27
	v_cvt_pknorm_i16_f32 v6, v6, v7
	v_mul_f32_e32 v7, v3, v28
	v_mul_f32_e32 v8, v3, v29
	v_cvt_pknorm_i16_f32 v7, v7, v8
	v_mul_f32_e32 v8, v3, v30
	v_mul_f32_e32 v9, v3, v31
	v_cvt_pknorm_i16_f32 v8, v8, v9
	v_mul_f32_e32 v9, v3, v32
	v_mul_f32_e32 v3, v3, v33
	s_waitcnt lgkmcnt(0)
	v_max_f32_e32 v13, v13, v44
	v_cvt_pknorm_i16_f32 v9, v9, v3
	v_rcp_f32_e32 v3, v13
	v_cmp_lt_f32_e32 vcc, 0, v13
	s_mov_b64 s[6:7], 0x5400
	v_lshl_add_u64 v[10:11], v[4:5], 0, s[6:7]
	v_cndmask_b32_e32 v3, 0, v3, vcc
	global_store_dwordx4 v[10:11], v[6:9], off sc0 sc1
	s_nop 1
	v_mul_f32_e32 v6, v3, v34
	v_mul_f32_e32 v7, v3, v35
	v_cvt_pknorm_i16_f32 v6, v6, v7
	v_mul_f32_e32 v7, v3, v36
	v_mul_f32_e32 v8, v3, v37
	v_cvt_pknorm_i16_f32 v7, v7, v8
	v_mul_f32_e32 v8, v3, v38
	v_mul_f32_e32 v9, v3, v39
	v_cvt_pknorm_i16_f32 v8, v8, v9
	v_mul_f32_e32 v9, v3, v40
	v_mul_f32_e32 v3, v3, v41
	s_mov_b64 s[6:7], 0x5600
	v_cvt_pknorm_i16_f32 v9, v9, v3
	v_lshl_add_u64 v[10:11], v[4:5], 0, s[6:7]
	global_store_dwordx4 v[10:11], v[6:9], off sc0 sc1
	s_nop 1
	v_pk_mul_f32 v[6:7], v[12:13], s[4:5] op_sel_hi:[1,0]
	global_store_dwordx2 v0, v[6:7], s[2:3] offset:168
	v_accvgpr_read_b32 v3, a8
	v_accvgpr_read_b32 v6, a24
	v_accvgpr_read_b32 v7, a40
	v_max3_f32 v8, |v3|, |v6|, |v7|
	v_accvgpr_read_b32 v9, a56
	v_accvgpr_read_b32 v14, a72
	v_max3_f32 v8, |v8|, |v9|, |v14|
	v_accvgpr_read_b32 v15, a120
	v_accvgpr_read_b32 v16, a136
	v_max3_f32 v8, |v8|, |v15|, |v16|
	v_accvgpr_read_b32 v10, a88
	v_accvgpr_read_b32 v17, a88
	v_max3_f32 v8, |v8|, |v17|, |v10|
	v_accvgpr_read_b32 v18, a9
	v_accvgpr_read_b32 v19, a25
	v_accvgpr_read_b32 v20, a41
	v_max3_f32 v10, |v18|, |v19|, |v20|
	v_accvgpr_read_b32 v21, a57
	v_accvgpr_read_b32 v22, a73
	v_max3_f32 v10, |v10|, |v21|, |v22|
	v_accvgpr_read_b32 v23, a121
	v_accvgpr_read_b32 v24, a137
	v_max3_f32 v10, |v10|, |v23|, |v24|
	v_accvgpr_read_b32 v11, a89
	v_accvgpr_read_b32 v25, a89
	v_max3_f32 v11, |v10|, |v25|, |v11|
	v_accvgpr_read_b32 v26, a10
	v_accvgpr_read_b32 v27, a26
	v_accvgpr_read_b32 v28, a42
	v_max3_f32 v10, |v26|, |v27|, |v28|
	v_accvgpr_read_b32 v29, a58
	v_accvgpr_read_b32 v30, a74
	v_max3_f32 v10, |v10|, |v29|, |v30|
	v_accvgpr_read_b32 v31, a122
	v_accvgpr_read_b32 v32, a138
	v_max3_f32 v10, |v10|, |v31|, |v32|
	v_accvgpr_read_b32 v12, a90
	v_accvgpr_read_b32 v33, a90
	v_max3_f32 v12, |v10|, |v33|, |v12|
	v_accvgpr_read_b32 v34, a11
	v_accvgpr_read_b32 v35, a27
	v_accvgpr_read_b32 v36, a43
	v_max3_f32 v10, |v34|, |v35|, |v36|
	v_accvgpr_read_b32 v37, a59
	v_accvgpr_read_b32 v38, a75
	v_max3_f32 v10, |v10|, |v37|, |v38|
	v_accvgpr_read_b32 v13, a91
	v_accvgpr_read_b32 v39, a123
	v_accvgpr_read_b32 v40, a139
	v_max3_f32 v10, |v10|, |v39|, |v40|
	v_accvgpr_read_b32 v41, a91
	v_max3_f32 v13, |v10|, |v41|, |v13|
	s_mov_b64 s[6:7], 0x6000
	s_nop 1
	v_max_f32_dpp v8, v8, v8 quad_perm:[1,0,3,2] row_mask:0xf bank_mask:0xf
	v_max_f32_dpp v11, v11, v11 quad_perm:[1,0,3,2] row_mask:0xf bank_mask:0xf
	v_max_f32_dpp v12, v12, v12 quad_perm:[1,0,3,2] row_mask:0xf bank_mask:0xf
	v_max_f32_dpp v13, v13, v13 quad_perm:[1,0,3,2] row_mask:0xf bank_mask:0xf
	v_max_f32_dpp v8, v8, v8 quad_perm:[2,3,0,1] row_mask:0xf bank_mask:0xf
	v_max_f32_dpp v11, v11, v11 quad_perm:[2,3,0,1] row_mask:0xf bank_mask:0xf
	v_max_f32_dpp v12, v12, v12 quad_perm:[2,3,0,1] row_mask:0xf bank_mask:0xf
	v_max_f32_dpp v13, v13, v13 quad_perm:[2,3,0,1] row_mask:0xf bank_mask:0xf
	v_max_f32_dpp v8, v8, v8 row_half_mirror row_mask:0xf bank_mask:0xf
	v_max_f32_dpp v11, v11, v11 row_half_mirror row_mask:0xf bank_mask:0xf
	v_max_f32_dpp v12, v12, v12 row_half_mirror row_mask:0xf bank_mask:0xf
	v_max_f32_dpp v13, v13, v13 row_half_mirror row_mask:0xf bank_mask:0xf
	v_max_f32_dpp v8, v8, v8 row_mirror row_mask:0xf bank_mask:0xf
	v_max_f32_dpp v11, v11, v11 row_mirror row_mask:0xf bank_mask:0xf
	v_max_f32_dpp v12, v12, v12 row_mirror row_mask:0xf bank_mask:0xf
	v_max_f32_dpp v13, v13, v13 row_mirror row_mask:0xf bank_mask:0xf
	s_nop 0
	ds_swizzle_b32 v10, v8 offset:swizzle(SWAP,16)
	s_waitcnt lgkmcnt(0)
	v_max_f32_e32 v10, v8, v10
	ds_swizzle_b32 v42, v11 offset:swizzle(SWAP,16)
	v_rcp_f32_e32 v8, v10
	v_cmp_lt_f32_e32 vcc, 0, v10
	s_waitcnt lgkmcnt(0)
	v_max_f32_e32 v11, v11, v42
	ds_swizzle_b32 v43, v12 offset:swizzle(SWAP,16)
	s_waitcnt lgkmcnt(0)
	v_max_f32_e32 v12, v12, v43
	ds_swizzle_b32 v44, v13 offset:swizzle(SWAP,16)
	v_cndmask_b32_e32 v42, 0, v8, vcc
	v_mul_f32_e32 v3, v42, v3
	v_mul_f32_e32 v6, v42, v6
	v_cvt_pknorm_i16_f32 v6, v3, v6
	v_mul_f32_e32 v3, v42, v7
	v_mul_f32_e32 v7, v42, v9
	v_cvt_pknorm_i16_f32 v7, v3, v7
	v_mul_f32_e32 v3, v42, v14
	v_mul_f32_e32 v8, v42, v15
	v_cvt_pknorm_i16_f32 v8, v3, v8
	v_mul_f32_e32 v3, v42, v16
	v_mul_f32_e32 v9, v42, v17
	v_cvt_pknorm_i16_f32 v9, v3, v9
	v_rcp_f32_e32 v3, v11
	v_cmp_lt_f32_e32 vcc, 0, v11
	v_lshl_add_u64 v[14:15], v[4:5], 0, s[6:7]
	global_store_dwordx4 v[14:15], v[6:9], off sc0 sc1
	s_nop 1
	s_mov_b64 s[6:7], 0x6200
	v_cndmask_b32_e32 v3, 0, v3, vcc
	v_mul_f32_e32 v6, v3, v18
	v_mul_f32_e32 v7, v3, v19
	v_cvt_pknorm_i16_f32 v6, v6, v7
	v_mul_f32_e32 v7, v3, v20
	v_mul_f32_e32 v8, v3, v21
	v_cvt_pknorm_i16_f32 v7, v7, v8
	v_mul_f32_e32 v8, v3, v22
	v_mul_f32_e32 v9, v3, v23
	v_cvt_pknorm_i16_f32 v8, v8, v9
	v_mul_f32_e32 v9, v3, v24
	v_mul_f32_e32 v3, v3, v25
	v_cvt_pknorm_i16_f32 v9, v9, v3
	v_rcp_f32_e32 v3, v12
	v_cmp_lt_f32_e32 vcc, 0, v12
	v_lshl_add_u64 v[14:15], v[4:5], 0, s[6:7]
	global_store_dwordx4 v[14:15], v[6:9], off sc0 sc1
	s_nop 1
	v_pk_mul_f32 v[6:7], v[10:11], s[4:5] op_sel_hi:[1,0]
	v_cndmask_b32_e32 v3, 0, v3, vcc
	global_store_dwordx2 v0, v[6:7], s[2:3] offset:192
	v_mul_f32_e32 v6, v3, v26
	v_mul_f32_e32 v7, v3, v27
	v_cvt_pknorm_i16_f32 v6, v6, v7
	v_mul_f32_e32 v7, v3, v28
	v_mul_f32_e32 v8, v3, v29
	v_cvt_pknorm_i16_f32 v7, v7, v8
	v_mul_f32_e32 v8, v3, v30
	v_mul_f32_e32 v9, v3, v31
	v_cvt_pknorm_i16_f32 v8, v8, v9
	v_mul_f32_e32 v9, v3, v32
	v_mul_f32_e32 v3, v3, v33
	s_waitcnt lgkmcnt(0)
	v_max_f32_e32 v13, v13, v44
	v_cvt_pknorm_i16_f32 v9, v9, v3
	v_rcp_f32_e32 v3, v13
	v_cmp_lt_f32_e32 vcc, 0, v13
	s_mov_b64 s[6:7], 0x6400
	v_lshl_add_u64 v[10:11], v[4:5], 0, s[6:7]
	v_cndmask_b32_e32 v3, 0, v3, vcc
	global_store_dwordx4 v[10:11], v[6:9], off sc0 sc1
	s_nop 1
	v_mul_f32_e32 v6, v3, v34
	v_mul_f32_e32 v7, v3, v35
	v_cvt_pknorm_i16_f32 v6, v6, v7
	v_mul_f32_e32 v7, v3, v36
	v_mul_f32_e32 v8, v3, v37
	v_cvt_pknorm_i16_f32 v7, v7, v8
	v_mul_f32_e32 v8, v3, v38
	v_mul_f32_e32 v9, v3, v39
	v_cvt_pknorm_i16_f32 v8, v8, v9
	v_mul_f32_e32 v9, v3, v40
	v_mul_f32_e32 v3, v3, v41
	s_mov_b64 s[6:7], 0x6600
	v_cvt_pknorm_i16_f32 v9, v9, v3
	v_lshl_add_u64 v[10:11], v[4:5], 0, s[6:7]
	global_store_dwordx4 v[10:11], v[6:9], off sc0 sc1
	s_nop 1
	v_pk_mul_f32 v[6:7], v[12:13], s[4:5] op_sel_hi:[1,0]
	global_store_dwordx2 v0, v[6:7], s[2:3] offset:200
	v_accvgpr_read_b32 v3, a12
	v_accvgpr_read_b32 v6, a28
	v_accvgpr_read_b32 v7, a44
	v_max3_f32 v8, |v3|, |v6|, |v7|
	v_accvgpr_read_b32 v9, a60
	v_accvgpr_read_b32 v14, a76
	v_max3_f32 v8, |v8|, |v9|, |v14|
	v_accvgpr_read_b32 v15, a124
	v_accvgpr_read_b32 v16, a140
	v_max3_f32 v8, |v8|, |v15|, |v16|
	v_accvgpr_read_b32 v10, a92
	v_accvgpr_read_b32 v17, a92
	v_max3_f32 v8, |v8|, |v17|, |v10|
	v_accvgpr_read_b32 v18, a13
	v_accvgpr_read_b32 v19, a29
	v_accvgpr_read_b32 v20, a45
	v_max3_f32 v10, |v18|, |v19|, |v20|
	v_accvgpr_read_b32 v21, a61
	v_accvgpr_read_b32 v22, a77
	v_max3_f32 v10, |v10|, |v21|, |v22|
	v_accvgpr_read_b32 v23, a125
	v_accvgpr_read_b32 v24, a141
	v_max3_f32 v10, |v10|, |v23|, |v24|
	v_accvgpr_read_b32 v11, a93
	v_accvgpr_read_b32 v25, a93
	v_max3_f32 v11, |v10|, |v25|, |v11|
	v_accvgpr_read_b32 v26, a14
	v_accvgpr_read_b32 v27, a30
	v_accvgpr_read_b32 v28, a46
	v_max3_f32 v10, |v26|, |v27|, |v28|
	v_accvgpr_read_b32 v29, a62
	v_accvgpr_read_b32 v30, a78
	v_max3_f32 v10, |v10|, |v29|, |v30|
	v_accvgpr_read_b32 v31, a126
	v_accvgpr_read_b32 v32, a142
	v_max3_f32 v10, |v10|, |v31|, |v32|
	v_accvgpr_read_b32 v12, a94
	v_accvgpr_read_b32 v33, a94
	v_max3_f32 v12, |v10|, |v33|, |v12|
	v_accvgpr_read_b32 v34, a15
	v_accvgpr_read_b32 v35, a31
	v_accvgpr_read_b32 v36, a47
	v_max3_f32 v10, |v34|, |v35|, |v36|
	v_accvgpr_read_b32 v37, a63
	v_accvgpr_read_b32 v38, a79
	v_max3_f32 v10, |v10|, |v37|, |v38|
	v_accvgpr_read_b32 v13, a95
	v_accvgpr_read_b32 v39, a127
	v_accvgpr_read_b32 v40, a143
	v_max3_f32 v10, |v10|, |v39|, |v40|
	v_accvgpr_read_b32 v41, a95
	v_max3_f32 v13, |v10|, |v41|, |v13|
	s_mov_b64 s[6:7], 0x7000
	s_nop 1
	v_max_f32_dpp v8, v8, v8 quad_perm:[1,0,3,2] row_mask:0xf bank_mask:0xf
	v_max_f32_dpp v11, v11, v11 quad_perm:[1,0,3,2] row_mask:0xf bank_mask:0xf
	v_max_f32_dpp v12, v12, v12 quad_perm:[1,0,3,2] row_mask:0xf bank_mask:0xf
	v_max_f32_dpp v13, v13, v13 quad_perm:[1,0,3,2] row_mask:0xf bank_mask:0xf
	v_max_f32_dpp v8, v8, v8 quad_perm:[2,3,0,1] row_mask:0xf bank_mask:0xf
	v_max_f32_dpp v11, v11, v11 quad_perm:[2,3,0,1] row_mask:0xf bank_mask:0xf
	v_max_f32_dpp v12, v12, v12 quad_perm:[2,3,0,1] row_mask:0xf bank_mask:0xf
	v_max_f32_dpp v13, v13, v13 quad_perm:[2,3,0,1] row_mask:0xf bank_mask:0xf
	v_max_f32_dpp v8, v8, v8 row_half_mirror row_mask:0xf bank_mask:0xf
	v_max_f32_dpp v11, v11, v11 row_half_mirror row_mask:0xf bank_mask:0xf
	v_max_f32_dpp v12, v12, v12 row_half_mirror row_mask:0xf bank_mask:0xf
	v_max_f32_dpp v13, v13, v13 row_half_mirror row_mask:0xf bank_mask:0xf
	v_max_f32_dpp v8, v8, v8 row_mirror row_mask:0xf bank_mask:0xf
	v_max_f32_dpp v11, v11, v11 row_mirror row_mask:0xf bank_mask:0xf
	v_max_f32_dpp v12, v12, v12 row_mirror row_mask:0xf bank_mask:0xf
	v_max_f32_dpp v13, v13, v13 row_mirror row_mask:0xf bank_mask:0xf
	s_nop 0
	ds_swizzle_b32 v10, v8 offset:swizzle(SWAP,16)
	s_waitcnt lgkmcnt(0)
	v_max_f32_e32 v10, v8, v10
	ds_swizzle_b32 v42, v11 offset:swizzle(SWAP,16)
	v_rcp_f32_e32 v8, v10
	v_cmp_lt_f32_e32 vcc, 0, v10
	s_waitcnt lgkmcnt(0)
	v_max_f32_e32 v11, v11, v42
	ds_swizzle_b32 v43, v12 offset:swizzle(SWAP,16)
	s_waitcnt lgkmcnt(0)
	v_max_f32_e32 v12, v12, v43
	ds_swizzle_b32 v44, v13 offset:swizzle(SWAP,16)
	v_cndmask_b32_e32 v42, 0, v8, vcc
	v_mul_f32_e32 v3, v42, v3
	v_mul_f32_e32 v6, v42, v6
	v_cvt_pknorm_i16_f32 v6, v3, v6
	v_mul_f32_e32 v3, v42, v7
	v_mul_f32_e32 v7, v42, v9
	v_cvt_pknorm_i16_f32 v7, v3, v7
	v_mul_f32_e32 v3, v42, v14
	v_mul_f32_e32 v8, v42, v15
	v_cvt_pknorm_i16_f32 v8, v3, v8
	v_mul_f32_e32 v3, v42, v16
	v_mul_f32_e32 v9, v42, v17
	v_cvt_pknorm_i16_f32 v9, v3, v9
	v_rcp_f32_e32 v3, v11
	v_cmp_lt_f32_e32 vcc, 0, v11
	v_lshl_add_u64 v[14:15], v[4:5], 0, s[6:7]
	global_store_dwordx4 v[14:15], v[6:9], off sc0 sc1
	s_nop 1
	s_mov_b64 s[6:7], 0x7200
	v_cndmask_b32_e32 v3, 0, v3, vcc
	v_mul_f32_e32 v6, v3, v18
	v_mul_f32_e32 v7, v3, v19
	v_cvt_pknorm_i16_f32 v6, v6, v7
	v_mul_f32_e32 v7, v3, v20
	v_mul_f32_e32 v8, v3, v21
	v_cvt_pknorm_i16_f32 v7, v7, v8
	v_mul_f32_e32 v8, v3, v22
	v_mul_f32_e32 v9, v3, v23
	v_cvt_pknorm_i16_f32 v8, v8, v9
	v_mul_f32_e32 v9, v3, v24
	v_mul_f32_e32 v3, v3, v25
	v_cvt_pknorm_i16_f32 v9, v9, v3
	v_rcp_f32_e32 v3, v12
	v_cmp_lt_f32_e32 vcc, 0, v12
	v_lshl_add_u64 v[14:15], v[4:5], 0, s[6:7]
	global_store_dwordx4 v[14:15], v[6:9], off sc0 sc1
	s_nop 1
	v_pk_mul_f32 v[6:7], v[10:11], s[4:5] op_sel_hi:[1,0]
	v_cndmask_b32_e32 v3, 0, v3, vcc
	global_store_dwordx2 v0, v[6:7], s[2:3] offset:224
	v_mul_f32_e32 v6, v3, v26
	v_mul_f32_e32 v7, v3, v27
	v_cvt_pknorm_i16_f32 v6, v6, v7
	v_mul_f32_e32 v7, v3, v28
	v_mul_f32_e32 v8, v3, v29
	v_cvt_pknorm_i16_f32 v7, v7, v8
	v_mul_f32_e32 v8, v3, v30
	v_mul_f32_e32 v9, v3, v31
	v_cvt_pknorm_i16_f32 v8, v8, v9
	v_mul_f32_e32 v9, v3, v32
	v_mul_f32_e32 v3, v3, v33
	s_waitcnt lgkmcnt(0)
	v_max_f32_e32 v13, v13, v44
	v_cvt_pknorm_i16_f32 v9, v9, v3
	v_rcp_f32_e32 v3, v13
	v_cmp_lt_f32_e32 vcc, 0, v13
	s_mov_b64 s[6:7], 0x7400
	v_lshl_add_u64 v[10:11], v[4:5], 0, s[6:7]
	v_cndmask_b32_e32 v3, 0, v3, vcc
	global_store_dwordx4 v[10:11], v[6:9], off sc0 sc1
	s_nop 1
	v_mul_f32_e32 v6, v3, v34
	v_mul_f32_e32 v7, v3, v35
	v_cvt_pknorm_i16_f32 v6, v6, v7
	v_mul_f32_e32 v7, v3, v36
	v_mul_f32_e32 v8, v3, v37
	v_cvt_pknorm_i16_f32 v7, v7, v8
	v_mul_f32_e32 v8, v3, v38
	v_mul_f32_e32 v9, v3, v39
	v_cvt_pknorm_i16_f32 v8, v8, v9
	v_mul_f32_e32 v9, v3, v40
	v_mul_f32_e32 v3, v3, v41
	s_mov_b64 s[6:7], 0x7600
	v_cvt_pknorm_i16_f32 v9, v9, v3
	v_lshl_add_u64 v[4:5], v[4:5], 0, s[6:7]
	global_store_dwordx4 v[4:5], v[6:9], off sc0 sc1
	s_nop 1
	v_pk_mul_f32 v[4:5], v[12:13], s[4:5] op_sel_hi:[1,0]
	global_store_dwordx2 v0, v[4:5], s[2:3] offset:232
	ds_bpermute_b32 v4, v133, v134
	s_lshl_b64 s[0:1], s[0:1], 2
	s_add_u32 s0, s26, s0
	s_addc_u32 s1, s27, s1
	v_mov_b32_e32 v3, v1
	v_cmp_gt_i32_e32 vcc, 32, v132
	v_lshl_add_u64 v[0:1], s[0:1], 0, v[2:3]
	s_and_saveexec_b64 s[0:1], vcc
	s_cbranch_execz .LBB1_6
	s_waitcnt lgkmcnt(0)
	v_add_f32_e32 v2, v134, v4
	global_store_dword v[0:1], v2, off

	.amdhsa_kernel _Z6k_mainPKDF16_PKfS2_S2_PKmPjPfS6_
		.amdhsa_group_segment_fixed_size 114688
		.amdhsa_private_segment_fixed_size 0
		.amdhsa_kernarg_size 64
		.amdhsa_user_sgpr_count 2
		.amdhsa_user_sgpr_dispatch_ptr 0
		.amdhsa_user_sgpr_queue_ptr 0
		.amdhsa_user_sgpr_kernarg_segment_ptr 1
		.amdhsa_user_sgpr_dispatch_id 0
		.amdhsa_user_sgpr_kernarg_preload_length 0
		.amdhsa_user_sgpr_kernarg_preload_offset 0
		.amdhsa_user_sgpr_private_segment_size 0
		.amdhsa_uses_dynamic_stack 0
		.amdhsa_enable_private_segment 0
		.amdhsa_system_sgpr_workgroup_id_x 1
		.amdhsa_system_sgpr_workgroup_id_y 0
		.amdhsa_system_sgpr_workgroup_id_z 0
		.amdhsa_system_sgpr_workgroup_info 0
		.amdhsa_system_vgpr_workitem_id 0
		.amdhsa_next_free_vgpr 480
		.amdhsa_next_free_sgpr 96
		.amdhsa_accum_offset 224
		.amdhsa_reserve_vcc 1
		.amdhsa_float_round_mode_32 0
		.amdhsa_float_round_mode_16_64 0
		.amdhsa_float_denorm_mode_32 3
		.amdhsa_float_denorm_mode_16_64 3
		.amdhsa_dx10_clamp 1
		.amdhsa_ieee_mode 1
		.amdhsa_fp16_overflow 0
		.amdhsa_tg_split 0
		.amdhsa_exception_fp_ieee_invalid_op 0
		.amdhsa_exception_fp_denorm_src 0
		.amdhsa_exception_fp_ieee_div_zero 0
		.amdhsa_exception_fp_ieee_overflow 0
		.amdhsa_exception_fp_ieee_underflow 0
		.amdhsa_exception_fp_ieee_inexact 0
		.amdhsa_exception_int_div_zero 0
	.end_amdhsa_kernel

	.text
	.protected	_Z9k_redprepILi1EEvPKfPKjS1_S1_S1_S1_S1_PfPKDv8_DF16_S7_S1_PDF16_S4_S4_S4_PKiS7_S1_S1_S1_S4_S4_
	.globl	_Z9k_redprepILi1EEvPKfPKjS1_S1_S1_S1_S1_PfPKDv8_DF16_S7_S1_PDF16_S4_S4_S4_PKiS7_S1_S1_S1_S4_S4_
	.p2align	8
	.type	_Z9k_redprepILi1EEvPKfPKjS1_S1_S1_S1_S1_PfPKDv8_DF16_S7_S1_PDF16_S4_S4_S4_PKiS7_S1_S1_S1_S4_S4_,@function

	.amdhsa_kernel _Z9k_redprepILi1EEvPKfPKjS1_S1_S1_S1_S1_PfPKDv8_DF16_S7_S1_PDF16_S4_S4_S4_PKiS7_S1_S1_S1_S4_S4_
		.amdhsa_group_segment_fixed_size 53792
		.amdhsa_private_segment_fixed_size 0
		.amdhsa_kernarg_size 176
		.amdhsa_user_sgpr_count 2
		.amdhsa_user_sgpr_dispatch_ptr 0
		.amdhsa_user_sgpr_queue_ptr 0
		.amdhsa_user_sgpr_kernarg_segment_ptr 1
		.amdhsa_user_sgpr_dispatch_id 0
		.amdhsa_user_sgpr_kernarg_preload_length 0
		.amdhsa_user_sgpr_kernarg_preload_offset 0
		.amdhsa_user_sgpr_private_segment_size 0
		.amdhsa_uses_dynamic_stack 0
		.amdhsa_enable_private_segment 0
		.amdhsa_system_sgpr_workgroup_id_x 1
		.amdhsa_system_sgpr_workgroup_id_y 0
		.amdhsa_system_sgpr_workgroup_id_z 0
		.amdhsa_system_sgpr_workgroup_info 0
		.amdhsa_system_vgpr_workitem_id 0
		.amdhsa_next_free_vgpr 103
		.amdhsa_next_free_sgpr 100
		.amdhsa_accum_offset 104
		.amdhsa_reserve_vcc 1
		.amdhsa_float_round_mode_32 0
		.amdhsa_float_round_mode_16_64 0
		.amdhsa_float_denorm_mode_32 3
		.amdhsa_float_denorm_mode_16_64 3
		.amdhsa_dx10_clamp 1
		.amdhsa_ieee_mode 1
		.amdhsa_fp16_overflow 0
		.amdhsa_tg_split 0
		.amdhsa_exception_fp_ieee_invalid_op 0
		.amdhsa_exception_fp_denorm_src 0
		.amdhsa_exception_fp_ieee_div_zero 0
		.amdhsa_exception_fp_ieee_overflow 0
		.amdhsa_exception_fp_ieee_underflow 0
		.amdhsa_exception_fp_ieee_inexact 0
		.amdhsa_exception_int_div_zero 0
	.end_amdhsa_kernel
	.text
.Lfunc_end3:
	.size	_Z9k_redprepILi1EEvPKfPKjS1_S1_S1_S1_S1_PfPKDv8_DF16_S7_S1_PDF16_S4_S4_S4_PKiS7_S1_S1_S1_S4_S4_, .Lfunc_end3-_Z9k_redprepILi1EEvPKfPKjS1_S1_S1_S1_S1_PfPKDv8_DF16_S7_S1_PDF16_S4_S4_S4_PKiS7_S1_S1_S1_S4_S4_
	.set _Z9k_redprepILi1EEvPKfPKjS1_S1_S1_S1_S1_PfPKDv8_DF16_S7_S1_PDF16_S4_S4_S4_PKiS7_S1_S1_S1_S4_S4_.num_vgpr, 103
	.set _Z9k_redprepILi1EEvPKfPKjS1_S1_S1_S1_S1_PfPKDv8_DF16_S7_S1_PDF16_S4_S4_S4_PKiS7_S1_S1_S1_S4_S4_.num_agpr, 0
	.set _Z9k_redprepILi1EEvPKfPKjS1_S1_S1_S1_S1_PfPKDv8_DF16_S7_S1_PDF16_S4_S4_S4_PKiS7_S1_S1_S1_S4_S4_.numbered_sgpr, 100
	.set _Z9k_redprepILi1EEvPKfPKjS1_S1_S1_S1_S1_PfPKDv8_DF16_S7_S1_PDF16_S4_S4_S4_PKiS7_S1_S1_S1_S4_S4_.num_named_barrier, 0
	.set _Z9k_redprepILi1EEvPKfPKjS1_S1_S1_S1_S1_PfPKDv8_DF16_S7_S1_PDF16_S4_S4_S4_PKiS7_S1_S1_S1_S4_S4_.private_seg_size, 0
	.set _Z9k_redprepILi1EEvPKfPKjS1_S1_S1_S1_S1_PfPKDv8_DF16_S7_S1_PDF16_S4_S4_S4_PKiS7_S1_S1_S1_S4_S4_.uses_vcc, 1
	.set _Z9k_redprepILi1EEvPKfPKjS1_S1_S1_S1_S1_PfPKDv8_DF16_S7_S1_PDF16_S4_S4_S4_PKiS7_S1_S1_S1_S4_S4_.uses_flat_scratch, 0
	.set _Z9k_redprepILi1EEvPKfPKjS1_S1_S1_S1_S1_PfPKDv8_DF16_S7_S1_PDF16_S4_S4_S4_PKiS7_S1_S1_S1_S4_S4_.has_dyn_sized_stack, 0
	.set _Z9k_redprepILi1EEvPKfPKjS1_S1_S1_S1_S1_PfPKDv8_DF16_S7_S1_PDF16_S4_S4_S4_PKiS7_S1_S1_S1_S4_S4_.has_recursion, 0
	.set _Z9k_redprepILi1EEvPKfPKjS1_S1_S1_S1_S1_PfPKDv8_DF16_S7_S1_PDF16_S4_S4_S4_PKiS7_S1_S1_S1_S4_S4_.has_indirect_call, 0

	.text
	.protected	_Z9k_redprepILi2EEvPKfPKjS1_S1_S1_S1_S1_PfPKDv8_DF16_S7_S1_PDF16_S4_S4_S4_PKiS7_S1_S1_S1_S4_S4_
	.globl	_Z9k_redprepILi2EEvPKfPKjS1_S1_S1_S1_S1_PfPKDv8_DF16_S7_S1_PDF16_S4_S4_S4_PKiS7_S1_S1_S1_S4_S4_
	.p2align	8
	.type	_Z9k_redprepILi2EEvPKfPKjS1_S1_S1_S1_S1_PfPKDv8_DF16_S7_S1_PDF16_S4_S4_S4_PKiS7_S1_S1_S1_S4_S4_,@function

	.amdhsa_kernel _Z9k_redprepILi2EEvPKfPKjS1_S1_S1_S1_S1_PfPKDv8_DF16_S7_S1_PDF16_S4_S4_S4_PKiS7_S1_S1_S1_S4_S4_
		.amdhsa_group_segment_fixed_size 66688
		.amdhsa_private_segment_fixed_size 0
		.amdhsa_kernarg_size 176
		.amdhsa_user_sgpr_count 2
		.amdhsa_user_sgpr_dispatch_ptr 0
		.amdhsa_user_sgpr_queue_ptr 0
		.amdhsa_user_sgpr_kernarg_segment_ptr 1
		.amdhsa_user_sgpr_dispatch_id 0
		.amdhsa_user_sgpr_kernarg_preload_length 0
		.amdhsa_user_sgpr_kernarg_preload_offset 0
		.amdhsa_user_sgpr_private_segment_size 0
		.amdhsa_uses_dynamic_stack 0
		.amdhsa_enable_private_segment 0
		.amdhsa_system_sgpr_workgroup_id_x 1
		.amdhsa_system_sgpr_workgroup_id_y 0
		.amdhsa_system_sgpr_workgroup_id_z 0
		.amdhsa_system_sgpr_workgroup_info 0
		.amdhsa_system_vgpr_workitem_id 0
		.amdhsa_next_free_vgpr 106
		.amdhsa_next_free_sgpr 96
		.amdhsa_accum_offset 108
		.amdhsa_reserve_vcc 1
		.amdhsa_float_round_mode_32 0
		.amdhsa_float_round_mode_16_64 0
		.amdhsa_float_denorm_mode_32 3
		.amdhsa_float_denorm_mode_16_64 3
		.amdhsa_dx10_clamp 1
		.amdhsa_ieee_mode 1
		.amdhsa_fp16_overflow 0
		.amdhsa_tg_split 0
		.amdhsa_exception_fp_ieee_invalid_op 0
		.amdhsa_exception_fp_denorm_src 0
		.amdhsa_exception_fp_ieee_div_zero 0
		.amdhsa_exception_fp_ieee_overflow 0
		.amdhsa_exception_fp_ieee_underflow 0
		.amdhsa_exception_fp_ieee_inexact 0
		.amdhsa_exception_int_div_zero 0
	.end_amdhsa_kernel
	.text
.Lfunc_end4:
	.size	_Z9k_redprepILi2EEvPKfPKjS1_S1_S1_S1_S1_PfPKDv8_DF16_S7_S1_PDF16_S4_S4_S4_PKiS7_S1_S1_S1_S4_S4_, .Lfunc_end4-_Z9k_redprepILi2EEvPKfPKjS1_S1_S1_S1_S1_PfPKDv8_DF16_S7_S1_PDF16_S4_S4_S4_PKiS7_S1_S1_S1_S4_S4_
	.set _Z9k_redprepILi2EEvPKfPKjS1_S1_S1_S1_S1_PfPKDv8_DF16_S7_S1_PDF16_S4_S4_S4_PKiS7_S1_S1_S1_S4_S4_.num_vgpr, 106
	.set _Z9k_redprepILi2EEvPKfPKjS1_S1_S1_S1_S1_PfPKDv8_DF16_S7_S1_PDF16_S4_S4_S4_PKiS7_S1_S1_S1_S4_S4_.num_agpr, 0
	.set _Z9k_redprepILi2EEvPKfPKjS1_S1_S1_S1_S1_PfPKDv8_DF16_S7_S1_PDF16_S4_S4_S4_PKiS7_S1_S1_S1_S4_S4_.numbered_sgpr, 96
	.set _Z9k_redprepILi2EEvPKfPKjS1_S1_S1_S1_S1_PfPKDv8_DF16_S7_S1_PDF16_S4_S4_S4_PKiS7_S1_S1_S1_S4_S4_.num_named_barrier, 0
	.set _Z9k_redprepILi2EEvPKfPKjS1_S1_S1_S1_S1_PfPKDv8_DF16_S7_S1_PDF16_S4_S4_S4_PKiS7_S1_S1_S1_S4_S4_.private_seg_size, 0
	.set _Z9k_redprepILi2EEvPKfPKjS1_S1_S1_S1_S1_PfPKDv8_DF16_S7_S1_PDF16_S4_S4_S4_PKiS7_S1_S1_S1_S4_S4_.uses_vcc, 1
	.set _Z9k_redprepILi2EEvPKfPKjS1_S1_S1_S1_S1_PfPKDv8_DF16_S7_S1_PDF16_S4_S4_S4_PKiS7_S1_S1_S1_S4_S4_.uses_flat_scratch, 0
	.set _Z9k_redprepILi2EEvPKfPKjS1_S1_S1_S1_S1_PfPKDv8_DF16_S7_S1_PDF16_S4_S4_S4_PKiS7_S1_S1_S1_S4_S4_.has_dyn_sized_stack, 0
	.set _Z9k_redprepILi2EEvPKfPKjS1_S1_S1_S1_S1_PfPKDv8_DF16_S7_S1_PDF16_S4_S4_S4_PKiS7_S1_S1_S1_S4_S4_.has_recursion, 0
	.set _Z9k_redprepILi2EEvPKfPKjS1_S1_S1_S1_S1_PfPKDv8_DF16_S7_S1_PDF16_S4_S4_S4_PKiS7_S1_S1_S1_S4_S4_.has_indirect_call, 0

amdhsa.kernels:
  - .agpr_count:     0
    .args:
      - .actual_access:  read_only
        .address_space:  global
        .offset:         0
        .size:           8
        .value_kind:     global_buffer
      - .address_space:  global
        .offset:         8
        .size:           8
        .value_kind:     global_buffer
      - .actual_access:  read_only
        .address_space:  global
        .offset:         16
        .size:           8
        .value_kind:     global_buffer
      - .actual_access:  read_only
        .address_space:  global
        .offset:         24
        .size:           8
        .value_kind:     global_buffer
      - .actual_access:  read_only
        .address_space:  global
        .offset:         32
        .size:           8
        .value_kind:     global_buffer
      - .actual_access:  read_only
        .address_space:  global
        .offset:         40
        .size:           8
        .value_kind:     global_buffer
      - .actual_access:  read_only
        .address_space:  global
        .offset:         48
        .size:           8
        .value_kind:     global_buffer
      - .actual_access:  read_only
        .address_space:  global
        .offset:         56
        .size:           8
        .value_kind:     global_buffer
      - .actual_access:  write_only
        .address_space:  global
        .offset:         64
        .size:           8
        .value_kind:     global_buffer
      - .actual_access:  write_only
        .address_space:  global
        .offset:         72
        .size:           8
        .value_kind:     global_buffer
      - .actual_access:  write_only
        .address_space:  global
        .offset:         80
        .size:           8
        .value_kind:     global_buffer
      - .actual_access:  write_only
        .address_space:  global
        .offset:         88
        .size:           8
        .value_kind:     global_buffer
      - .actual_access:  read_only
        .address_space:  global
        .offset:         96
        .size:           8
        .value_kind:     global_buffer
      - .actual_access:  write_only
        .address_space:  global
        .offset:         104
        .size:           8
        .value_kind:     global_buffer
      - .actual_access:  read_only
        .address_space:  global
        .offset:         112
        .size:           8
        .value_kind:     global_buffer
      - .actual_access:  write_only
        .address_space:  global
        .offset:         120
        .size:           8
        .value_kind:     global_buffer
      - .actual_access:  write_only
        .address_space:  global
        .offset:         128
        .size:           8
        .value_kind:     global_buffer
      - .actual_access:  write_only
        .address_space:  global
        .offset:         136
        .size:           8
        .value_kind:     global_buffer
      - .actual_access:  write_only
        .address_space:  global
        .offset:         144
        .size:           8
        .value_kind:     global_buffer
    .group_segment_fixed_size: 4096
    .kernarg_segment_align: 8
    .kernarg_segment_size: 152
    .language:       OpenCL C
    .language_version:
      - 2
      - 0
    .max_flat_workgroup_size: 512
    .name:           _Z7k_frontPKfPmS0_S0_S0_S0_S0_S0_PDF16_S2_PfS3_S0_S2_S0_S2_S3_S3_S3_
    .private_segment_fixed_size: 0
    .sgpr_count:     88
    .sgpr_spill_count: 0
    .symbol:         _Z7k_frontPKfPmS0_S0_S0_S0_S0_S0_PDF16_S2_PfS3_S0_S2_S0_S2_S3_S3_S3_.kd
    .uniform_work_group_size: 1
    .uses_dynamic_stack: false
    .vgpr_count:     68
    .vgpr_spill_count: 0
    .wavefront_size: 64
  - .agpr_count:     256
    .args:
      - .actual_access:  read_only
        .address_space:  global
        .offset:         0
        .size:           8
        .value_kind:     global_buffer
      - .actual_access:  read_only
        .address_space:  global
        .offset:         8
        .size:           8
        .value_kind:     global_buffer
      - .actual_access:  read_only
        .address_space:  global
        .offset:         16
        .size:           8
        .value_kind:     global_buffer
      - .actual_access:  read_only
        .address_space:  global
        .offset:         24
        .size:           8
        .value_kind:     global_buffer
      - .actual_access:  read_only
        .address_space:  global
        .offset:         32
        .size:           8
        .value_kind:     global_buffer
      - .address_space:  global
        .offset:         40
        .size:           8
        .value_kind:     global_buffer
      - .actual_access:  write_only
        .address_space:  global
        .offset:         48
        .size:           8
        .value_kind:     global_buffer
      - .actual_access:  write_only
        .address_space:  global
        .offset:         56
        .size:           8
        .value_kind:     global_buffer
    .group_segment_fixed_size: 114688
    .kernarg_segment_align: 8
    .kernarg_segment_size: 64
    .language:       OpenCL C
    .language_version:
      - 2
      - 0
    .max_flat_workgroup_size: 256
    .name:           _Z6k_mainPKDF16_PKfS2_S2_PKmPjPfS6_
    .private_segment_fixed_size: 0
    .sgpr_count:     99
    .sgpr_spill_count: 0
    .symbol:         _Z6k_mainPKDF16_PKfS2_S2_PKmPjPfS6_.kd
    .uniform_work_group_size: 1
    .uses_dynamic_stack: false
    .vgpr_count:     480
    .vgpr_spill_count: 0
    .wavefront_size: 64
  - .agpr_count:     0
    .args:
      - .actual_access:  read_only
        .address_space:  global
        .offset:         0
        .size:           8
        .value_kind:     global_buffer
      - .actual_access:  read_only
        .address_space:  global
        .offset:         8
        .size:           8
        .value_kind:     global_buffer
      - .actual_access:  read_only
        .address_space:  global
        .offset:         16
        .size:           8
        .value_kind:     global_buffer
      - .actual_access:  read_only
        .address_space:  global
        .offset:         24
        .size:           8
        .value_kind:     global_buffer
      - .actual_access:  read_only
        .address_space:  global
        .offset:         32
        .size:           8
        .value_kind:     global_buffer
      - .actual_access:  read_only
        .address_space:  global
        .offset:         40
        .size:           8
        .value_kind:     global_buffer
      - .actual_access:  read_only
        .address_space:  global
        .offset:         48
        .size:           8
        .value_kind:     global_buffer
      - .actual_access:  read_only
        .address_space:  global
        .offset:         56
        .size:           8
        .value_kind:     global_buffer
      - .actual_access:  read_only
        .address_space:  global
        .offset:         64
        .size:           8
        .value_kind:     global_buffer
      - .actual_access:  write_only
        .address_space:  global
        .offset:         72
        .size:           8
        .value_kind:     global_buffer
      - .actual_access:  write_only
        .address_space:  global
        .offset:         80
        .size:           8
        .value_kind:     global_buffer
    .group_segment_fixed_size: 101632
    .kernarg_segment_align: 8
    .kernarg_segment_size: 88
    .language:       OpenCL C
    .language_version:
      - 2
      - 0
    .max_flat_workgroup_size: 256
    .name:           _Z7k_graphPKfS0_S0_S0_S0_S0_S0_S0_S0_PfS1_
    .private_segment_fixed_size: 0
    .sgpr_count:     25
    .sgpr_spill_count: 0
    .symbol:         _Z7k_graphPKfS0_S0_S0_S0_S0_S0_S0_S0_PfS1_.kd
    .uniform_work_group_size: 1
    .uses_dynamic_stack: false
    .vgpr_count:     118
    .vgpr_spill_count: 0
    .wavefront_size: 64
  - .agpr_count:     0
    .args:
      - .actual_access:  read_only
        .address_space:  global
        .offset:         0
        .size:           8
        .value_kind:     global_buffer
      - .actual_access:  read_only
        .address_space:  global
        .offset:         8
        .size:           8
        .value_kind:     global_buffer
      - .actual_access:  read_only
        .address_space:  global
        .offset:         16
        .size:           8
        .value_kind:     global_buffer
      - .actual_access:  read_only
        .address_space:  global
        .offset:         24
        .size:           8
        .value_kind:     global_buffer
      - .actual_access:  read_only
        .address_space:  global
        .offset:         32
        .size:           8
        .value_kind:     global_buffer
      - .actual_access:  read_only
        .address_space:  global
        .offset:         40
        .size:           8
        .value_kind:     global_buffer
      - .actual_access:  read_only
        .address_space:  global
        .offset:         48
        .size:           8
        .value_kind:     global_buffer
      - .address_space:  global
        .offset:         56
        .size:           8
        .value_kind:     global_buffer
      - .actual_access:  read_only
        .address_space:  global
        .offset:         64
        .size:           8
        .value_kind:     global_buffer
      - .actual_access:  read_only
        .address_space:  global
        .offset:         72
        .size:           8
        .value_kind:     global_buffer
      - .actual_access:  read_only
        .address_space:  global
        .offset:         80
        .size:           8
        .value_kind:     global_buffer
      - .address_space:  global
        .offset:         88
        .size:           8
        .value_kind:     global_buffer
      - .actual_access:  write_only
        .address_space:  global
        .offset:         96
        .size:           8
        .value_kind:     global_buffer
      - .actual_access:  write_only
        .address_space:  global
        .offset:         104
        .size:           8
        .value_kind:     global_buffer
      - .actual_access:  write_only
        .address_space:  global
        .offset:         112
        .size:           8
        .value_kind:     global_buffer
      - .actual_access:  read_only
        .address_space:  global
        .offset:         120
        .size:           8
        .value_kind:     global_buffer
      - .actual_access:  read_only
        .address_space:  global
        .offset:         128
        .size:           8
        .value_kind:     global_buffer
      - .actual_access:  read_only
        .address_space:  global
        .offset:         136
        .size:           8
        .value_kind:     global_buffer
      - .actual_access:  read_only
        .address_space:  global
        .offset:         144
        .size:           8
        .value_kind:     global_buffer
      - .actual_access:  read_only
        .address_space:  global
        .offset:         152
        .size:           8
        .value_kind:     global_buffer
      - .actual_access:  read_only
        .address_space:  global
        .offset:         160
        .size:           8
        .value_kind:     global_buffer
      - .actual_access:  read_only
        .address_space:  global
        .offset:         168
        .size:           8
        .value_kind:     global_buffer
    .group_segment_fixed_size: 53792
    .kernarg_segment_align: 8
    .kernarg_segment_size: 176
    .language:       OpenCL C
    .language_version:
      - 2
      - 0
    .max_flat_workgroup_size: 512
    .name:           _Z9k_redprepILi1EEvPKfPKjS1_S1_S1_S1_S1_PfPKDv8_DF16_S7_S1_PDF16_S4_S4_S4_PKiS7_S1_S1_S1_S4_S4_
    .private_segment_fixed_size: 0
    .sgpr_count:     106
    .sgpr_spill_count: 4
    .symbol:         _Z9k_redprepILi1EEvPKfPKjS1_S1_S1_S1_S1_PfPKDv8_DF16_S7_S1_PDF16_S4_S4_S4_PKiS7_S1_S1_S1_S4_S4_.kd
    .uniform_work_group_size: 1
    .uses_dynamic_stack: false
    .vgpr_count:     103
    .vgpr_spill_count: 0
    .wavefront_size: 64
  - .agpr_count:     0
    .args:
      - .actual_access:  read_only
        .address_space:  global
        .offset:         0
        .size:           8
        .value_kind:     global_buffer
      - .actual_access:  read_only
        .address_space:  global
        .offset:         8
        .size:           8
        .value_kind:     global_buffer
      - .actual_access:  read_only
        .address_space:  global
        .offset:         16
        .size:           8
        .value_kind:     global_buffer
      - .actual_access:  read_only
        .address_space:  global
        .offset:         24
        .size:           8
        .value_kind:     global_buffer
      - .actual_access:  read_only
        .address_space:  global
        .offset:         32
        .size:           8
        .value_kind:     global_buffer
      - .actual_access:  read_only
        .address_space:  global
        .offset:         40
        .size:           8
        .value_kind:     global_buffer
      - .actual_access:  read_only
        .address_space:  global
        .offset:         48
        .size:           8
        .value_kind:     global_buffer
      - .address_space:  global
        .offset:         56
        .size:           8
        .value_kind:     global_buffer
      - .actual_access:  read_only
        .address_space:  global
        .offset:         64
        .size:           8
        .value_kind:     global_buffer
      - .actual_access:  read_only
        .address_space:  global
        .offset:         72
        .size:           8
        .value_kind:     global_buffer
      - .actual_access:  read_only
        .address_space:  global
        .offset:         80
        .size:           8
        .value_kind:     global_buffer
      - .actual_access:  read_only
        .address_space:  global
        .offset:         88
        .size:           8
        .value_kind:     global_buffer
      - .actual_access:  read_only
        .address_space:  global
        .offset:         96
        .size:           8
        .value_kind:     global_buffer
      - .actual_access:  read_only
        .address_space:  global
        .offset:         104
        .size:           8
        .value_kind:     global_buffer
      - .actual_access:  read_only
        .address_space:  global
        .offset:         112
        .size:           8
        .value_kind:     global_buffer
      - .actual_access:  read_only
        .address_space:  global
        .offset:         120
        .size:           8
        .value_kind:     global_buffer
      - .actual_access:  read_only
        .address_space:  global
        .offset:         128
        .size:           8
        .value_kind:     global_buffer
      - .actual_access:  read_only
        .address_space:  global
        .offset:         136
        .size:           8
        .value_kind:     global_buffer
      - .actual_access:  read_only
        .address_space:  global
        .offset:         144
        .size:           8
        .value_kind:     global_buffer
      - .actual_access:  read_only
        .address_space:  global
        .offset:         152
        .size:           8
        .value_kind:     global_buffer
      - .actual_access:  write_only
        .address_space:  global
        .offset:         160
        .size:           8
        .value_kind:     global_buffer
      - .address_space:  global
        .offset:         168
        .size:           8
        .value_kind:     global_buffer
    .group_segment_fixed_size: 66688
    .kernarg_segment_align: 8
    .kernarg_segment_size: 176
    .language:       OpenCL C
    .language_version:
      - 2
      - 0
    .max_flat_workgroup_size: 512
    .name:           _Z9k_redprepILi2EEvPKfPKjS1_S1_S1_S1_S1_PfPKDv8_DF16_S7_S1_PDF16_S4_S4_S4_PKiS7_S1_S1_S1_S4_S4_
    .private_segment_fixed_size: 0
    .sgpr_count:     102
    .sgpr_spill_count: 0
    .symbol:         _Z9k_redprepILi2EEvPKfPKjS1_S1_S1_S1_S1_PfPKDv8_DF16_S7_S1_PDF16_S4_S4_S4_PKiS7_S1_S1_S1_S4_S4_.kd
    .uniform_work_group_size: 1
    .uses_dynamic_stack: false
    .vgpr_count:     106
    .vgpr_spill_count: 0
    .wavefront_size: 64
